# q_route key staging: p.sk1/p.sk2 base pointers loaded once per phase with a scalar load and selected per iteration instead of 16 dependent vector pointer loads (each with a full wait) per tile
# baseline (speedup 1.0000x reference)
; __device__ __forceinline__ int opaque_tid() { int t = threadIdx.x; asm volatile("" : "+v"(t)); return t; }
; __device__ void phase_q_route(KParams& p, int bid, int nb, char* smem) {
;   const int tid = opaque_tid(), lane = tid & 63, w = tid >> 6;
;   const int wm = w >> 1, wn = w & 1, lr = lane & 15, lq = lane >> 4;
;   const int l31 = lane & 31, lh = lane >> 5;
;   for (int tile0 = bid; tile0 < 512; tile0 += nb) {
;     const int tile = ((nb & 7) == 0 && nb >= 512) ? (((tile0 & 7) * 8 + ((tile0 >> 3) & 7)) * 8 + (tile0 >> 6)) : tile0;
;     const int h = tile & 7, m0 = (tile >> 3) * 128;
;     ...
;           const bf16x8 qb = *reinterpret_cast<const bf16x8*>(smem + swz16(w * 32 + l31, sd * 8 + ks * 2 + lh));
; #pragma unroll
;           for (int i = 0; i < 2; ++i) {
;             const bf16x8 ka = *reinterpret_cast<const bf16x8*>(smem + 32768 + swz8(sd * 128 + (ih * 2 + i) * 32 + l31, ks * 2 + lh));
;             Sa[i] = __builtin_amdgcn_mfma_f32_32x32x16_bf16(ka, qb, Sa[i], 0, 0, 0);
;           }
;         }
; #pragma unroll
;         for (int i = 0; i < 2; ++i) {
;           uint32_t Kg[16];
; #pragma unroll
;           for (int g2 = 0; g2 < 16; ++g2)
;             Kg[g2] = (mono_key(Sa[i][g2]) & ~0x7Fu) | (uint32_t)((ih * 2 + i) * 32 + (g2 & 3) + 8 * (g2 >> 2)) | kb;
.Lgb_wd_9:
.LBB0_1183:
	s_or_b64 exec, exec, s[8:9]
	v_mov_b32_e32 v253, 0x12818
	ds_read_b32 v253, v253
	s_waitcnt lgkmcnt(0)
	v_readfirstlane_b32 s2, v253
	s_nop 0
	s_mov_b64 s[10:11], s[0:1]
	s_waitcnt lgkmcnt(0)
	v_mov_b32_e32 v1, v0
	s_cmpk_gt_i32 s2, 0x1ff
	s_barrier
	s_cbranch_scc1 .LBB0_1196
	s_load_dwordx2 s[20:21], s[10:11], 0xf8
	s_load_dwordx2 s[12:13], s[10:11], 0x108
	s_load_dwordx4 s[64:67], s[10:11], 0xb8
	v_ashrrev_i32_e32 v2, 1, v1
	s_cmpk_gt_i32 s34, 0x1ff
	v_and_b32_e32 v2, 0xffffffc0, v2
	v_and_b32_e32 v6, 63, v1
	s_cselect_b64 s[8:9], -1, 0
	v_ashrrev_i32_e32 v3, 31, v2
	s_and_b64 s[22:23], s[8:9], s[48:49]
	s_waitcnt lgkmcnt(0)
	v_lshl_add_u64 v[4:5], v[2:3], 2, s[12:13]
	v_lshrrev_b32_e32 v3, 2, v1
	v_cmp_lt_u32_e64 s[8:9], 31, v6
	v_lshrrev_b32_e32 v6, 3, v1
	v_and_b32_e32 v8, 31, v1
	v_ashrrev_i32_e32 v10, 6, v1
	v_and_b32_e32 v11, 12, v3
	v_lshlrev_b32_e32 v12, 3, v1
	s_movk_i32 s3, 0x1100
	v_and_b32_e32 v6, 9, v6
	v_or_b32_e32 v2, v11, v2
	v_and_b32_e32 v76, 8, v12
	v_lshlrev_b32_e32 v12, 8, v8
	v_mul_lo_u32 v14, v10, s3
	s_movk_i32 s3, 0x88
	s_load_dwordx4 s[12:15], s[10:11], 0x138
	s_load_dwordx4 s[16:19], s[10:11], 0x240
	v_or_b32_e32 v16, 2, v6
	v_or_b32_e32 v20, 4, v6
	v_or_b32_e32 v24, 6, v6
	v_bfe_u32 v7, v1, 5, 1
	v_and_b32_e32 v9, 15, v1
	v_lshlrev_b32_e32 v66, 2, v11
	v_mov_b32_e32 v67, 0
	v_lshl_or_b32 v12, v10, 13, v12
	v_and_b32_e32 v13, 7, v1
	v_mad_u32_u24 v78, v8, s3, v14
	v_lshl_or_b32 v79, v10, 5, v8
	v_lshlrev_b32_e32 v2, 8, v2
	v_bitop3_b32 v3, v3, v6, 12 bitop3:0x6c
	v_bitop3_b32 v10, v11, v6, 1 bitop3:0x36
	v_bitop3_b32 v14, v11, v6, 2 bitop3:0x36
	v_bitop3_b32 v15, v11, v6, 3 bitop3:0x36
	v_bitop3_b32 v17, v6, v11, 2 bitop3:0x36
	v_bitop3_b32 v18, v11, v16, 1 bitop3:0x36
	v_bitop3_b32 v19, v11, v6, 2 bitop3:0x14
	v_bitop3_b32 v16, v11, v16, 3 bitop3:0x36
	v_bitop3_b32 v21, v6, v11, 4 bitop3:0x36
	v_bitop3_b32 v22, v11, v20, 1 bitop3:0x36
	v_bitop3_b32 v23, v11, v20, 2 bitop3:0x36
	v_bitop3_b32 v20, v11, v20, 3 bitop3:0x36
	v_bitop3_b32 v6, v6, v11, 6 bitop3:0x36
	v_bitop3_b32 v25, v11, v24, 1 bitop3:0x36
	v_bitop3_b32 v26, v11, v24, 2 bitop3:0x36
	v_bitop3_b32 v11, v11, v24, 3 bitop3:0x36
	v_lshl_add_u64 v[68:69], v[4:5], 0, v[66:67]
	v_lshlrev_b32_e32 v4, 1, v1
	v_lshlrev_b32_e32 v77, 2, v7
	v_lshl_or_b32 v3, v3, 4, v2
	v_lshl_or_b32 v10, v10, 4, v2
	v_lshl_or_b32 v14, v14, 4, v2
	v_lshl_or_b32 v15, v15, 4, v2
	v_lshl_or_b32 v17, v17, 4, v2
	v_lshl_or_b32 v18, v18, 4, v2
	v_lshl_or_b32 v19, v19, 4, v2
	v_lshl_or_b32 v16, v16, 4, v2
	v_lshl_or_b32 v21, v21, 4, v2
	v_lshl_or_b32 v22, v22, 4, v2
	v_lshl_or_b32 v23, v23, 4, v2
	v_lshl_or_b32 v20, v20, 4, v2
	v_lshl_or_b32 v6, v6, 4, v2
	v_lshl_or_b32 v25, v25, 4, v2
	v_lshl_or_b32 v26, v26, 4, v2
	v_lshl_or_b32 v2, v11, 4, v2
	v_bitop3_b32 v11, v7, v1, 15 bitop3:0x78
	v_bitop3_b32 v24, v7, v1, 7 bitop3:0x78
	v_bitop3_b32 v27, v7, v9, 2 bitop3:0x36
	v_bitop3_b32 v28, v7, v13, 2 bitop3:0x36
	v_bitop3_b32 v29, v7, v9, 4 bitop3:0x36
	v_bitop3_b32 v30, v7, v13, 4 bitop3:0x36
	v_bitop3_b32 v31, v7, v9, 6 bitop3:0x36
	v_bitop3_b32 v13, v7, v13, 6 bitop3:0x36
	v_bitop3_b32 v32, v7, v9, 8 bitop3:0x36
	v_bitop3_b32 v33, v7, v9, 10 bitop3:0x36
	v_bitop3_b32 v34, v7, v9, 12 bitop3:0x36
	v_bitop3_b32 v7, v7, v9, 14 bitop3:0x36
	v_and_b32_e32 v4, 14, v4
	v_lshlrev_b32_e32 v5, 2, v9
	v_lshlrev_b32_e32 v8, 7, v8
	v_lshlrev_b32_e32 v11, 4, v11
	v_lshlrev_b32_e32 v24, 4, v24
	v_lshlrev_b32_e32 v27, 4, v27
	v_lshlrev_b32_e32 v28, 4, v28
	v_lshlrev_b32_e32 v29, 4, v29
	v_lshlrev_b32_e32 v30, 4, v30
	v_lshlrev_b32_e32 v31, 4, v31
	v_lshlrev_b32_e32 v13, 4, v13
	v_lshlrev_b32_e32 v32, 4, v32
	v_lshlrev_b32_e32 v33, 4, v33
	v_lshlrev_b32_e32 v34, 4, v34
	v_lshlrev_b32_e32 v7, 4, v7
	v_and_b32_e32 v74, 0x4f, v1
	v_bfe_u32 v75, v1, 1, 3
	v_or_b32_e32 v80, 1, v77
	v_or_b32_e32 v81, 2, v77
	v_or_b32_e32 v82, 3, v77
	v_or_b32_e32 v83, 8, v77
	v_or_b32_e32 v84, 9, v77
	v_or_b32_e32 v85, 10, v77
	v_or_b32_e32 v86, 11, v77
	v_or_b32_e32 v87, 16, v77
	v_or_b32_e32 v88, 17, v77
	v_or_b32_e32 v89, 18, v77
	v_or_b32_e32 v90, 19, v77
	v_or_b32_e32 v91, 24, v77
	v_or_b32_e32 v92, 25, v77
	v_or_b32_e32 v93, 26, v77
	v_or_b32_e32 v94, 27, v77
	v_or_b32_e32 v95, 32, v77
	v_or_b32_e32 v96, 33, v77
	v_or_b32_e32 v97, 35, v77
	v_or_b32_e32 v98, 34, v77
	v_or_b32_e32 v99, 43, v77
	v_or_b32_e32 v100, 42, v77
	v_or_b32_e32 v101, 40, v77
	v_or_b32_e32 v102, 41, v77
	v_or_b32_e32 v103, 59, v77
	v_or_b32_e32 v104, 58, v77
	v_or_b32_e32 v105, 56, v77
	v_or_b32_e32 v106, 57, v77
	v_or_b32_e32 v107, 48, v77
	v_or_b32_e32 v108, 49, v77
	v_or_b32_e32 v109, 51, v77
	v_or_b32_e32 v110, 50, v77
	v_or_b32_e32 v111, 64, v77
	v_or_b32_e32 v112, 0x41, v77
	v_or_b32_e32 v113, 0x43, v77
	v_or_b32_e32 v114, 0x42, v77
	v_or_b32_e32 v115, 0x4b, v77
	v_or_b32_e32 v116, 0x4a, v77
	v_or_b32_e32 v117, 0x48, v77
	v_or_b32_e32 v118, 0x49, v77
	v_or_b32_e32 v119, 0x5b, v77
	v_or_b32_e32 v120, 0x5a, v77
	v_or_b32_e32 v121, 0x58, v77
	v_or_b32_e32 v122, 0x59, v77
	v_or_b32_e32 v123, 0x50, v77
	v_or_b32_e32 v124, 0x51, v77
	v_or_b32_e32 v125, 0x53, v77
	v_or_b32_e32 v126, 0x52, v77
	v_or_b32_e32 v127, 0x60, v77
	v_or_b32_e32 v128, 0x61, v77
	v_or_b32_e32 v129, 0x63, v77
	v_or_b32_e32 v130, 0x62, v77
	v_or_b32_e32 v131, 0x6b, v77
	v_or_b32_e32 v132, 0x6a, v77
	v_or_b32_e32 v133, 0x68, v77
	v_or_b32_e32 v134, 0x69, v77
	v_or_b32_e32 v135, 0x7b, v77
	v_or_b32_e32 v136, 0x7a, v77
	v_or_b32_e32 v137, 0x78, v77
	v_or_b32_e32 v138, 0x79, v77
	v_or_b32_e32 v139, 0x70, v77
	v_or_b32_e32 v140, 0x71, v77
	v_or_b32_e32 v141, 0x73, v77
	v_or_b32_e32 v142, 0x72, v77
	s_movk_i32 s3, 0xff80
	s_mov_b64 s[24:25], 0x10000
	s_mov_b64 s[26:27], 0x20000
	s_mov_b64 s[28:29], 0x30000
	s_mov_b32 s35, 0x1ffffc0
	s_mov_b64 s[30:31], 0x80
	s_mov_b64 s[36:37], 0x10080
	s_mov_b64 s[38:39], 0x20080
	s_mov_b64 s[40:41], 0x30080
	v_add_u32_e32 v143, v3, v4
	v_add_u32_e32 v144, v10, v4
	v_add_u32_e32 v145, v14, v4
	v_add_u32_e32 v146, v15, v4
	v_add_u32_e32 v147, v17, v4
	v_add_u32_e32 v148, v18, v4
	v_add_u32_e32 v149, v19, v4
	v_add_u32_e32 v150, v16, v4
	v_add_u32_e32 v151, v21, v4
	v_add_u32_e32 v152, v22, v4
	v_add_u32_e32 v153, v23, v4
	v_add_u32_e32 v154, v20, v4
	v_add_u32_e32 v155, v6, v4
	v_add_u32_e32 v156, v25, v4
	v_add_u32_e32 v157, v26, v4
	v_add_u32_e32 v158, v2, v4
	s_movk_i32 s46, 0x80
	v_lshlrev_b32_e32 v159, 2, v5
	v_add_u32_e32 v160, v12, v11
	v_add_u32_e32 v161, v24, v8
	v_add_u32_e32 v162, v12, v27
	v_add_u32_e32 v163, v28, v8
	v_add_u32_e32 v164, v12, v29
	v_add_u32_e32 v165, v30, v8
	v_add_u32_e32 v166, v12, v31
	v_add_u32_e32 v167, v13, v8
	v_add_u32_e32 v168, v12, v32
	v_add_u32_e32 v169, v12, v33
	v_add_u32_e32 v170, v12, v34
	v_add_u32_e32 v171, v12, v7
	s_movk_i32 s47, 0xff00
	v_mov_b32_e32 v172, 0xc0
	v_mov_b32_e32 v173, 0xb8
	v_bfrev_b32_e32 v174, 1
	s_branch .LBB0_1186

; __device__ void phase_q_route(KParams& p, int bid, int nb, char* smem) {
;     ...
; #pragma unroll 4
;     for (int r = 0; r < 16; ++r) {
;       const int id = tid + 256 * r, row = id >> 4, c4 = id & 15;
;       const float* src = ((row < 128) ? p.sk1 : p.sk2) + ((size_t)(h * 128 + (row & 127)) * 64 + c4 * 4);
;       const float4 v = *reinterpret_cast<const float4*>(src);
;       uint2 pk; pk.x = pack2(v.x, v.y); pk.y = pack2(v.z, v.w);
;       *reinterpret_cast<uint2*>(smem + 32768 + swz8(row, c4 >> 1) + (c4 & 1) * 8) = pk;
;     }
;     __syncthreads();
;     uint32_t L1[16], L2[16];
; #pragma unroll
;     for (int sd = 0; sd < 2; ++sd) {
;       uint32_t Lk[16];
; #pragma unroll
;       for (int i = 0; i < 16; ++i) Lk[i] = 0u;
;       const uint32_t kb = (uint32_t)(lh * 4);
; #pragma unroll
;       for (int ih = 0; ih < 2; ++ih) {
;         f32x16 Sa[2];
; #pragma unroll
;         for (int i = 0; i < 2; ++i)
; #pragma unroll
;           for (int g2 = 0; g2 < 16; ++g2) Sa[i][g2] = 0.f;
; #pragma unroll
;         for (int ks = 0; ks < 4; ++ks) {
;           const bf16x8 qb = *reinterpret_cast<const bf16x8*>(smem + swz16(w * 32 + l31, sd * 8 + ks * 2 + lh));
; #pragma unroll
;           for (int i = 0; i < 2; ++i) {
;             const bf16x8 ka = *reinterpret_cast<const bf16x8*>(smem + 32768 + swz8(sd * 128 + (ih * 2 + i) * 32 + l31, ks * 2 + lh));
;             Sa[i] = __builtin_amdgcn_mfma_f32_32x32x16_bf16(ka, qb, Sa[i], 0, 0, 0);
;           }
.LBB0_1189:
	s_cmpk_lt_u32 s43, 0x800
	s_cselect_b32 s68, s64, s66
	s_cselect_b32 s69, s65, s67
	v_add_u32_e32 v8, s43, v1
	v_ashrrev_i32_e32 v18, 4, v8
	v_cmp_gt_i32_e32 vcc, s46, v18
	v_add_u32_e32 v4, 0x100, v8
	v_and_b32_e32 v5, 0x7f, v18
	v_ashrrev_i32_e32 v19, 4, v4
	v_or_b32_e32 v4, s51, v5
	v_cmp_gt_i32_e32 vcc, s46, v19
	v_lshl_or_b32 v66, v4, 8, v159
	v_add_u32_e32 v6, 0x200, v8
	v_ashrrev_i32_e32 v20, 4, v6
	v_and_b32_e32 v6, 0x7f, v19
	v_or_b32_e32 v6, s51, v6
	v_add_u32_e32 v8, 0x300, v8
	v_ashrrev_i32_e32 v21, 4, v8
	v_and_b32_e32 v8, 0x7f, v20
	v_or_b32_e32 v8, s51, v8
	v_lshlrev_b32_e32 v22, 7, v18
	v_bitop3_b32 v18, v18, v75, 7 bitop3:0x6c
	v_lshlrev_b32_e32 v18, 4, v18
	v_lshlrev_b32_e32 v23, 7, v19
	v_bitop3_b32 v19, v19, v75, 7 bitop3:0x6c
	v_lshlrev_b32_e32 v24, 7, v20
	v_or3_b32 v18, v18, v22, v76
	v_lshlrev_b32_e32 v19, 4, v19
	v_lshlrev_b32_e32 v25, 7, v21
	v_or3_b32 v19, v19, v23, v76
	s_addk_i32 s43, 0x400
	s_cmpk_eq_i32 s43, 0x1000
	v_lshl_add_u64 v[2:3], s[68:69], 0, v[66:67]
	v_cmp_gt_i32_e32 vcc, s46, v20
	v_lshl_or_b32 v66, v6, 8, v159
	v_bitop3_b32 v20, v20, v75, 7 bitop3:0x6c
	v_lshlrev_b32_e32 v20, 4, v20
	v_or3_b32 v20, v20, v24, v76
	v_lshl_add_u64 v[6:7], s[68:69], 0, v[66:67]
	v_cmp_gt_i32_e32 vcc, s46, v21
	v_lshl_or_b32 v66, v8, 8, v159
	v_lshl_add_u64 v[10:11], s[68:69], 0, v[66:67]
	v_and_b32_e32 v4, 0x7f, v21
	v_or_b32_e32 v16, s51, v4
	v_lshl_or_b32 v66, v16, 8, v159
	global_load_dwordx4 v[2:5], v[2:3], off
	s_nop 0
	global_load_dwordx4 v[6:9], v[6:7], off
	s_nop 0
	global_load_dwordx4 v[10:13], v[10:11], off
	v_bitop3_b32 v21, v21, v75, 7 bitop3:0x6c
	v_lshlrev_b32_e32 v21, 4, v21
	v_or3_b32 v21, v21, v25, v76
	v_lshl_add_u64 v[14:15], s[68:69], 0, v[66:67]
	global_load_dwordx4 v[14:17], v[14:15], off
	s_waitcnt vmcnt(3)
	v_cvt_pk_bf16_f32 v2, v2, v3
	v_cvt_pk_bf16_f32 v3, v4, v5
	ds_write_b64 v18, v[2:3] offset:32768
	s_waitcnt vmcnt(2)
	v_cvt_pk_bf16_f32 v2, v6, v7
	v_cvt_pk_bf16_f32 v3, v8, v9
	ds_write_b64 v19, v[2:3] offset:32768
	s_waitcnt vmcnt(1)
	v_cvt_pk_bf16_f32 v2, v10, v11
	v_cvt_pk_bf16_f32 v3, v12, v13
	ds_write_b64 v20, v[2:3] offset:32768
	s_waitcnt vmcnt(0)
	v_cvt_pk_bf16_f32 v2, v14, v15
	v_cvt_pk_bf16_f32 v3, v16, v17
	ds_write_b64 v21, v[2:3] offset:32768
	s_cbranch_scc0 .LBB0_1189
	s_waitcnt lgkmcnt(0)
	s_barrier
	ds_read_b128 v[2:5], v161 offset:32768
	ds_read_b128 v[34:37], v160
	ds_read_b128 v[18:21], v161 offset:36864
	ds_read_b128 v[42:45], v161 offset:40960
	s_waitcnt lgkmcnt(2)
	v_mfma_f32_32x32x16_bf16 v[2:17], v[2:5], v[34:37], 0
	ds_read_b128 v[46:49], v163 offset:32768
	ds_read_b128 v[38:41], v162
	ds_read_b128 v[54:57], v163 offset:36864
	ds_read_b128 v[50:53], v161 offset:61440
	v_cmp_lt_i32_e32 vcc, v181, v180
	s_nop 1
	v_cndmask_b32_e32 v66, v178, v181, vcc
	v_lshlrev_b32_e32 v71, 2, v66
	s_waitcnt lgkmcnt(2)
	v_mfma_f32_32x32x16_bf16 v[2:17], v[46:49], v[38:41], v[2:17]
	ds_read_b128 v[46:49], v165 offset:32768
	ds_read_b128 v[62:65], v164
	ds_read_b128 v[192:195], v167 offset:32768
	v_mfma_f32_32x32x16_bf16 v[18:33], v[18:21], v[34:37], 0
	s_waitcnt lgkmcnt(1)
	v_mfma_f32_32x32x16_bf16 v[2:17], v[46:49], v[62:65], v[2:17]
	ds_read_b128 v[58:61], v166
	ds_read_b128 v[196:199], v165 offset:36864
	ds_read_b128 v[200:203], v167 offset:36864
	ds_read_b128 v[46:49], v165 offset:61440
	s_waitcnt lgkmcnt(3)
	v_mfma_f32_32x32x16_bf16 v[2:17], v[192:195], v[58:61], v[2:17]
	v_mfma_f32_32x32x16_bf16 v[18:33], v[54:57], v[38:41], v[18:33]
	s_nop 10
	v_not_b32_e32 v66, v2
	v_or_b32_e32 v70, 0x80000000, v2
	v_cmp_gt_i32_e32 vcc, 0, v2
	v_not_b32_e32 v72, v3
	v_or_b32_e32 v73, 0x80000000, v3
	v_cndmask_b32_e32 v2, v70, v66, vcc
	v_cmp_gt_i32_e32 vcc, 0, v3
	s_waitcnt lgkmcnt(2)
	v_mfma_f32_32x32x16_bf16 v[18:33], v[196:199], v[62:65], v[18:33]
	v_not_b32_e32 v175, v4
	v_or_b32_e32 v176, 0x80000000, v4
	v_cndmask_b32_e32 v3, v73, v72, vcc
	v_cmp_gt_i32_e32 vcc, 0, v4
	v_not_b32_e32 v177, v5
	v_or_b32_e32 v183, 0x80000000, v5
	v_cndmask_b32_e32 v4, v176, v175, vcc
	v_cmp_gt_i32_e32 vcc, 0, v5
	v_not_b32_e32 v54, v6
	v_or_b32_e32 v55, 0x80000000, v6
	v_cndmask_b32_e32 v5, v183, v177, vcc
	v_cmp_gt_i32_e32 vcc, 0, v6
	v_not_b32_e32 v66, v7
	v_or_b32_e32 v70, 0x80000000, v7
	v_cndmask_b32_e32 v6, v55, v54, vcc
	v_cmp_gt_i32_e32 vcc, 0, v7
	s_waitcnt lgkmcnt(1)
; __device__ __forceinline__ uint32_t mono_key(float f) {
;   uint32_t u = __float_as_uint(f);
;   return (u & 0x80000000u) ? ~u : (u | 0x80000000u);
; }
; __device__ __forceinline__ void bitonic_sort16_desc(uint32_t (&K)[16]) {
; #pragma unroll
;   for (int k = 2; k <= 16; k <<= 1)
; #pragma unroll
;     for (int j = k >> 1; j >= 1; j >>= 1)
; #pragma unroll
;       for (int i = 0; i < 16; ++i) {
;         const int l = i ^ j;
;         if (l > i) { if ((i & k) == 0) ce_desc(K[i], K[l]); else ce_desc(K[l], K[i]); }
;       }
; }
; __device__ void phase_q_route(KParams& p, int bid, int nb, char* smem) {
;     ...
; #pragma unroll
;         for (int i = 0; i < 2; ++i) {
;           uint32_t Kg[16];
; #pragma unroll
;           for (int g2 = 0; g2 < 16; ++g2)
;             Kg[g2] = (mono_key(Sa[i][g2]) & ~0x7Fu) | (uint32_t)((ih * 2 + i) * 32 + (g2 & 3) + 8 * (g2 >> 2)) | kb;
;           bitonic_sort16_desc(Kg);
	v_mfma_f32_32x32x16_bf16 v[18:33], v[200:203], v[58:61], v[18:33]
	v_and_or_b32 v2, v2, s3, v77
	v_cndmask_b32_e32 v7, v70, v66, vcc
	v_not_b32_e32 v66, v8
	v_or_b32_e32 v70, 0x80000000, v8
	v_cmp_gt_i32_e32 vcc, 0, v8
	v_and_or_b32 v3, v3, s3, v80
	v_and_or_b32 v4, v4, s3, v81
	v_cndmask_b32_e32 v8, v70, v66, vcc
	v_not_b32_e32 v66, v9
	v_or_b32_e32 v70, 0x80000000, v9
	v_cmp_gt_i32_e32 vcc, 0, v9
	s_nop 0
	v_not_b32_e32 v185, v18
	v_or_b32_e32 v191, 0x80000000, v18
	v_cndmask_b32_e32 v9, v70, v66, vcc
	v_not_b32_e32 v66, v10
	v_or_b32_e32 v70, 0x80000000, v10
	v_cmp_gt_i32_e32 vcc, 0, v10
	v_or_b32_e32 v192, 0x80000000, v21
	v_not_b32_e32 v193, v25
	v_cndmask_b32_e32 v10, v70, v66, vcc
	v_not_b32_e32 v66, v11
	v_or_b32_e32 v70, 0x80000000, v11
	v_cmp_gt_i32_e32 vcc, 0, v11
	v_or_b32_e32 v194, 0x80000000, v25
	v_or_b32_e32 v195, 0x80000000, v22
	v_cndmask_b32_e32 v11, v70, v66, vcc
	v_not_b32_e32 v66, v12
	v_or_b32_e32 v70, 0x80000000, v12
	v_cmp_gt_i32_e32 vcc, 0, v12
	v_not_b32_e32 v197, v33
	v_or_b32_e32 v198, 0x80000000, v33
	v_cndmask_b32_e32 v12, v70, v66, vcc
	v_not_b32_e32 v66, v13
	v_or_b32_e32 v70, 0x80000000, v13
	v_cmp_gt_i32_e32 vcc, 0, v13
	v_or_b32_e32 v199, 0x80000000, v30
	v_not_b32_e32 v200, v26
	v_cndmask_b32_e32 v13, v70, v66, vcc
	v_not_b32_e32 v66, v14
	v_or_b32_e32 v70, 0x80000000, v14
	v_cmp_gt_i32_e32 vcc, 0, v14
	v_or_b32_e32 v201, 0x80000000, v26
	v_or_b32_e32 v202, 0x80000000, v29
	v_cndmask_b32_e32 v14, v70, v66, vcc
	v_not_b32_e32 v66, v15
	v_or_b32_e32 v70, 0x80000000, v15
	v_cmp_gt_i32_e32 vcc, 0, v15
	v_and_or_b32 v5, v5, s3, v82
	v_and_or_b32 v6, v6, s3, v83
	v_cndmask_b32_e32 v15, v70, v66, vcc
	v_not_b32_e32 v66, v16
	v_or_b32_e32 v70, 0x80000000, v16
	v_cmp_gt_i32_e32 vcc, 0, v16
	v_and_or_b32 v7, v7, s3, v84
	v_and_or_b32 v8, v8, s3, v85
	v_cndmask_b32_e32 v16, v70, v66, vcc
	v_not_b32_e32 v66, v17
	v_or_b32_e32 v70, 0x80000000, v17
	v_cmp_gt_i32_e32 vcc, 0, v17
	v_and_or_b32 v9, v9, s3, v86
	v_and_or_b32 v10, v10, s3, v87
	v_cndmask_b32_e32 v17, v70, v66, vcc
	v_cmp_gt_i32_e32 vcc, 0, v18
	v_and_or_b32 v11, v11, s3, v88
	v_and_or_b32 v12, v12, s3, v89
	v_cndmask_b32_e32 v18, v191, v185, vcc
	v_not_b32_e32 v185, v19
	v_or_b32_e32 v191, 0x80000000, v19
	v_cmp_gt_i32_e32 vcc, 0, v19
	v_and_or_b32 v18, v18, s3, v95
	v_and_or_b32 v13, v13, s3, v90
	v_cndmask_b32_e32 v19, v191, v185, vcc
	v_not_b32_e32 v191, v21
	v_cmp_gt_i32_e32 vcc, 0, v21
	v_and_or_b32 v19, v19, s3, v96
	v_max_u32_e32 v185, v18, v19
	v_cndmask_b32_e32 v21, v192, v191, vcc
	v_not_b32_e32 v191, v20
	v_or_b32_e32 v192, 0x80000000, v20
	v_cmp_gt_i32_e32 vcc, 0, v20
	v_and_or_b32 v21, v21, s3, v97
	v_min_u32_e32 v18, v18, v19
	v_cndmask_b32_e32 v20, v192, v191, vcc
	v_cmp_gt_i32_e32 vcc, 0, v25
	v_and_or_b32 v20, v20, s3, v98
	v_min_u32_e32 v191, v21, v20
	v_cndmask_b32_e32 v25, v194, v193, vcc
	v_not_b32_e32 v193, v24
	v_or_b32_e32 v194, 0x80000000, v24
	v_cmp_gt_i32_e32 vcc, 0, v24
	v_and_or_b32 v25, v25, s3, v99
	v_max_u32_e32 v19, v21, v20
	v_cndmask_b32_e32 v24, v194, v193, vcc
	v_not_b32_e32 v194, v22
	v_cmp_gt_i32_e32 vcc, 0, v22
	v_and_or_b32 v24, v24, s3, v100
	v_max_u32_e32 v193, v25, v24
	v_cndmask_b32_e32 v22, v195, v194, vcc
	v_not_b32_e32 v194, v23
	v_or_b32_e32 v195, 0x80000000, v23
	v_cmp_gt_i32_e32 vcc, 0, v23
	v_and_or_b32 v22, v22, s3, v101
	v_min_u32_e32 v24, v25, v24
	v_cndmask_b32_e32 v23, v195, v194, vcc
	v_cmp_gt_i32_e32 vcc, 0, v33
	v_and_or_b32 v23, v23, s3, v102
	v_min_u32_e32 v194, v22, v23
	v_cndmask_b32_e32 v33, v198, v197, vcc
	v_not_b32_e32 v197, v32
	v_or_b32_e32 v198, 0x80000000, v32
	v_cmp_gt_i32_e32 vcc, 0, v32
	v_and_or_b32 v33, v33, s3, v103
	v_max_u32_e32 v22, v22, v23
	v_cndmask_b32_e32 v32, v198, v197, vcc
	v_not_b32_e32 v198, v30
	v_cmp_gt_i32_e32 vcc, 0, v30
	v_and_or_b32 v32, v32, s3, v104
	v_max_u32_e32 v197, v33, v32
	v_cndmask_b32_e32 v30, v199, v198, vcc
	v_not_b32_e32 v198, v31
	v_or_b32_e32 v199, 0x80000000, v31
	v_cmp_gt_i32_e32 vcc, 0, v31
	v_and_or_b32 v30, v30, s3, v105
	v_min_u32_e32 v32, v33, v32
	v_cndmask_b32_e32 v31, v199, v198, vcc
	v_cmp_gt_i32_e32 vcc, 0, v26
	v_and_or_b32 v31, v31, s3, v106
	v_min_u32_e32 v198, v30, v31
	v_cndmask_b32_e32 v26, v201, v200, vcc
	v_not_b32_e32 v200, v27
	v_or_b32_e32 v201, 0x80000000, v27
	v_cmp_gt_i32_e32 vcc, 0, v27
	v_and_or_b32 v26, v26, s3, v107
	v_max_u32_e32 v30, v30, v31
	v_cndmask_b32_e32 v27, v201, v200, vcc
	v_not_b32_e32 v201, v29
	v_cmp_gt_i32_e32 vcc, 0, v29
	v_and_or_b32 v27, v27, s3, v108
	v_max_u32_e32 v200, v26, v27
	v_cndmask_b32_e32 v29, v202, v201, vcc
	v_not_b32_e32 v201, v28
	v_or_b32_e32 v202, 0x80000000, v28
	v_cmp_gt_i32_e32 vcc, 0, v28
	v_and_or_b32 v29, v29, s3, v109
	v_min_u32_e32 v26, v26, v27
	v_cndmask_b32_e32 v28, v202, v201, vcc
	v_and_or_b32 v28, v28, s3, v110
	v_min_u32_e32 v201, v29, v28
	v_max_u32_e32 v27, v29, v28
	v_and_or_b32 v14, v14, s3, v91
	v_and_or_b32 v15, v15, s3, v92
	v_and_or_b32 v16, v16, s3, v93
	v_and_or_b32 v17, v17, s3, v94
	v_max_u32_e32 v192, v185, v191
	v_max_u32_e32 v20, v18, v19
	v_min_u32_e32 v195, v193, v194
	v_min_u32_e32 v23, v24, v22
	v_min_u32_e32 v185, v185, v191
	v_min_u32_e32 v18, v18, v19
	v_max_u32_e32 v191, v193, v194
	v_max_u32_e32 v22, v24, v22
	v_max_u32_e32 v199, v197, v198
	v_max_u32_e32 v31, v32, v30
	v_min_u32_e32 v202, v200, v201
	v_min_u32_e32 v28, v26, v27
	v_min_u32_e32 v197, v197, v198
	v_min_u32_e32 v30, v32, v30
	v_max_u32_e32 v198, v200, v201
	v_max_u32_e32 v26, v26, v27
	v_max_u32_e32 v66, v2, v3
	v_min_u32_e32 v2, v2, v3
	v_max_u32_e32 v3, v5, v4
	v_min_u32_e32 v4, v5, v4
	v_max_u32_e32 v5, v6, v7
	v_min_u32_e32 v6, v6, v7
	v_max_u32_e32 v7, v9, v8
; __device__ __forceinline__ void bitonic_sort16_desc(uint32_t (&K)[16]) {
; #pragma unroll
;   for (int k = 2; k <= 16; k <<= 1)
; #pragma unroll
;     for (int j = k >> 1; j >= 1; j >>= 1)
; #pragma unroll
;       for (int i = 0; i < 16; ++i) {
;         const int l = i ^ j;
;         if (l > i) { if ((i & k) == 0) ce_desc(K[i], K[l]); else ce_desc(K[l], K[i]); }
;       }
; }
	v_min_u32_e32 v8, v9, v8
	v_max_u32_e32 v9, v10, v11
	v_min_u32_e32 v10, v10, v11
	v_max_u32_e32 v11, v13, v12
	v_min_u32_e32 v12, v13, v12
	v_max_u32_e32 v13, v14, v15
	v_min_u32_e32 v14, v14, v15
	v_max_u32_e32 v15, v17, v16
	v_min_u32_e32 v16, v17, v16
	v_max_u32_e32 v21, v192, v20
	v_min_u32_e32 v25, v195, v23
	v_max_u32_e32 v19, v185, v18
	v_min_u32_e32 v24, v191, v22
	v_min_u32_e32 v20, v192, v20
	v_max_u32_e32 v23, v195, v23
	v_min_u32_e32 v18, v185, v18
	v_max_u32_e32 v22, v191, v22
	v_max_u32_e32 v33, v199, v31
	v_min_u32_e32 v29, v202, v28
	v_max_u32_e32 v32, v197, v30
	v_min_u32_e32 v27, v198, v26
	v_min_u32_e32 v31, v199, v31
	v_max_u32_e32 v28, v202, v28
	v_min_u32_e32 v30, v197, v30
	v_max_u32_e32 v26, v198, v26
	v_max_u32_e32 v17, v66, v4
	v_min_u32_e32 v4, v66, v4
	v_max_u32_e32 v66, v2, v3
	v_min_u32_e32 v2, v2, v3
	v_max_u32_e32 v3, v8, v5
	v_min_u32_e32 v5, v8, v5
	v_max_u32_e32 v8, v7, v6
	v_min_u32_e32 v6, v7, v6
	v_max_u32_e32 v7, v9, v12
	v_min_u32_e32 v9, v9, v12
	v_max_u32_e32 v12, v10, v11
	v_min_u32_e32 v10, v10, v11
	v_max_u32_e32 v11, v16, v13
	v_min_u32_e32 v13, v16, v13
	v_max_u32_e32 v16, v15, v14
	v_min_u32_e32 v14, v15, v14
	v_max_u32_e32 v196, v21, v25
	v_max_u32_e32 v193, v19, v24
	v_max_u32_e32 v192, v20, v23
	v_max_u32_e32 v185, v18, v22
	v_min_u32_e32 v203, v33, v29
	v_min_u32_e32 v200, v32, v27
	v_min_u32_e32 v199, v31, v28
	v_min_u32_e32 v197, v30, v26
	v_min_u32_e32 v21, v21, v25
	v_min_u32_e32 v19, v19, v24
	v_min_u32_e32 v20, v20, v23
	v_min_u32_e32 v18, v18, v22
	v_max_u32_e32 v25, v33, v29
	v_max_u32_e32 v27, v32, v27
	v_max_u32_e32 v28, v31, v28
	v_max_u32_e32 v26, v30, v26
	v_max_u32_e32 v15, v17, v66
	v_min_u32_e32 v17, v17, v66
	v_max_u32_e32 v66, v4, v2
	v_min_u32_e32 v2, v4, v2
	v_max_u32_e32 v4, v6, v5
	v_min_u32_e32 v5, v6, v5
	v_max_u32_e32 v6, v8, v3
	v_min_u32_e32 v3, v8, v3
	v_max_u32_e32 v8, v7, v12
	v_min_u32_e32 v7, v7, v12
	v_max_u32_e32 v12, v9, v10
	v_min_u32_e32 v9, v9, v10
	v_max_u32_e32 v10, v14, v13
	v_min_u32_e32 v13, v14, v13
	v_max_u32_e32 v14, v16, v11
	v_min_u32_e32 v11, v16, v11
	v_max_u32_e32 v194, v196, v193
	v_max_u32_e32 v191, v192, v185
	v_min_u32_e32 v201, v203, v200
	v_min_u32_e32 v198, v199, v197
	v_max_u32_e32 v24, v21, v19
	v_max_u32_e32 v22, v20, v18
	v_min_u32_e32 v29, v25, v27
	v_min_u32_e32 v30, v28, v26
	v_min_u32_e32 v193, v196, v193
	v_min_u32_e32 v185, v192, v185
	v_max_u32_e32 v196, v203, v200
	v_max_u32_e32 v197, v199, v197
	v_min_u32_e32 v19, v21, v19
	v_min_u32_e32 v18, v20, v18
	v_max_u32_e32 v21, v25, v27
	v_max_u32_e32 v25, v28, v26
	v_max_u32_e32 v16, v15, v5
	v_min_u32_e32 v5, v15, v5
	v_max_u32_e32 v15, v17, v4
	v_min_u32_e32 v4, v17, v4
	v_max_u32_e32 v17, v66, v3
	v_min_u32_e32 v3, v66, v3
	v_max_u32_e32 v66, v2, v6
	v_min_u32_e32 v2, v2, v6
	v_max_u32_e32 v6, v13, v8
	v_min_u32_e32 v8, v13, v8
	v_max_u32_e32 v13, v10, v7
	v_min_u32_e32 v7, v10, v7
	v_max_u32_e32 v10, v11, v12
	v_min_u32_e32 v11, v11, v12
	v_max_u32_e32 v12, v14, v9
	v_min_u32_e32 v9, v14, v9
	v_max_u32_e32 v195, v194, v191
	v_min_u32_e32 v202, v201, v198
	v_max_u32_e32 v23, v24, v22
	v_min_u32_e32 v31, v29, v30
	v_max_u32_e32 v192, v193, v185
	v_min_u32_e32 v199, v196, v197
	v_max_u32_e32 v20, v19, v18
	v_min_u32_e32 v26, v21, v25
	v_max_u32_e32 v14, v16, v17
	v_min_u32_e32 v16, v16, v17
	v_max_u32_e32 v17, v15, v66
	v_min_u32_e32 v15, v15, v66
	v_max_u32_e32 v66, v5, v3
	v_min_u32_e32 v3, v5, v3
	v_max_u32_e32 v5, v4, v2
	v_min_u32_e32 v2, v4, v2
	v_max_u32_e32 v4, v11, v8
	v_min_u32_e32 v8, v11, v8
	v_max_u32_e32 v11, v9, v7
	v_min_u32_e32 v7, v9, v7
	v_max_u32_e32 v9, v10, v6
	v_min_u32_e32 v6, v10, v6
	v_max_u32_e32 v10, v12, v13
	v_min_u32_e32 v12, v12, v13
	v_min_u32_e32 v204, v195, v202
	v_min_u32_e32 v32, v23, v31
	v_min_u32_e32 v200, v192, v199
	v_min_u32_e32 v27, v20, v26
	v_max_u32_e32 v13, v14, v17
	v_min_u32_e32 v14, v14, v17
	v_max_u32_e32 v17, v16, v15
	v_min_u32_e32 v15, v16, v15
	v_max_u32_e32 v16, v66, v5
	v_min_u32_e32 v5, v66, v5
	v_max_u32_e32 v66, v3, v2
	v_min_u32_e32 v2, v3, v2
	v_max_u32_e32 v3, v7, v8
	v_min_u32_e32 v7, v7, v8
	v_max_u32_e32 v8, v11, v4
	v_min_u32_e32 v4, v11, v4
	v_max_u32_e32 v11, v12, v6
	v_min_u32_e32 v6, v12, v6
	v_max_u32_e32 v12, v10, v9
	v_min_u32_e32 v9, v10, v9
	v_min_u32_e32 v33, v204, v32
	v_min_u32_e32 v28, v200, v27
	v_min_u32_e32 v191, v194, v191
	v_max_u32_e32 v194, v201, v198
	v_min_u32_e32 v22, v24, v22
	v_max_u32_e32 v24, v29, v30
	v_min_u32_e32 v185, v193, v185
	v_max_u32_e32 v193, v196, v197
	v_min_u32_e32 v18, v19, v18
	v_max_u32_e32 v19, v21, v25
	v_max_u32_e32 v32, v204, v32
	v_max_u32_e32 v27, v200, v27
	v_max_u32_e32 v10, v13, v7
	v_min_u32_e32 v7, v13, v7
	v_max_u32_e32 v13, v14, v3
	v_min_u32_e32 v3, v14, v3
	v_max_u32_e32 v14, v17, v4
	v_min_u32_e32 v4, v17, v4
	v_max_u32_e32 v17, v15, v8
	v_min_u32_e32 v8, v15, v8
	v_max_u32_e32 v15, v16, v6
	v_min_u32_e32 v6, v16, v6
	v_max_u32_e32 v16, v5, v11
	v_min_u32_e32 v5, v5, v11
	v_max_u32_e32 v11, v66, v9
	v_min_u32_e32 v9, v66, v9
	v_max_u32_e32 v66, v2, v12
	v_min_u32_e32 v2, v2, v12
	v_min_u32_e32 v203, v33, v28
	v_min_u32_e32 v198, v191, v194
	v_min_u32_e32 v29, v22, v24
	v_min_u32_e32 v196, v185, v193
	v_min_u32_e32 v21, v18, v19
	v_max_u32_e32 v28, v33, v28
	v_min_u32_e32 v33, v32, v27
	v_max_u32_e32 v27, v32, v27
	v_max_u32_e32 v32, v195, v202
	v_max_u32_e32 v23, v23, v31
	v_max_u32_e32 v192, v192, v199
	v_max_u32_e32 v20, v20, v26
	v_max_u32_e32 v191, v191, v194
	v_max_u32_e32 v22, v22, v24
	v_max_u32_e32 v185, v185, v193
	v_max_u32_e32 v18, v18, v19
	v_max_u32_e32 v12, v10, v15
	v_min_u32_e32 v10, v10, v15
	v_max_u32_e32 v15, v13, v16
; __device__ __forceinline__ void merge_top16(uint32_t (&Lk)[16], const uint32_t (&K)[16]) {
; #pragma unroll
;   for (int i = 0; i < 16; ++i) Lk[i] = max(Lk[i], K[15 - i]);
; #pragma unroll
;   for (int dd = 8; dd >= 1; dd >>= 1)
; #pragma unroll
;     for (int i = 0; i < 16; ++i)
;       if ((i & dd) == 0) ce_desc(Lk[i], Lk[i + dd]);
; }
; __device__ void phase_q_route(KParams& p, int bid, int nb, char* smem) {
;     ...
;         for (int ks = 0; ks < 4; ++ks) {
;           const bf16x8 qb = *reinterpret_cast<const bf16x8*>(smem + swz16(w * 32 + l31, sd * 8 + ks * 2 + lh));
; #pragma unroll
;           for (int i = 0; i < 2; ++i) {
;             const bf16x8 ka = *reinterpret_cast<const bf16x8*>(smem + 32768 + swz8(sd * 128 + (ih * 2 + i) * 32 + l31, ks * 2 + lh));
;             Sa[i] = __builtin_amdgcn_mfma_f32_32x32x16_bf16(ka, qb, Sa[i], 0, 0, 0);
;           }
	v_min_u32_e32 v13, v13, v16
	v_max_u32_e32 v16, v14, v11
	v_min_u32_e32 v11, v14, v11
	v_max_u32_e32 v14, v17, v66
	v_min_u32_e32 v17, v17, v66
	v_max_u32_e32 v66, v7, v6
	v_min_u32_e32 v6, v7, v6
	v_max_u32_e32 v7, v3, v5
	v_min_u32_e32 v3, v3, v5
	v_max_u32_e32 v5, v4, v9
	v_min_u32_e32 v4, v4, v9
	v_max_u32_e32 v9, v8, v2
	v_min_u32_e32 v30, v198, v29
	v_min_u32_e32 v25, v196, v21
	v_max_u32_e32 v29, v198, v29
	v_max_u32_e32 v21, v196, v21
	v_min_u32_e32 v31, v32, v23
	v_min_u32_e32 v26, v192, v20
	v_min_u32_e32 v24, v191, v22
	v_min_u32_e32 v19, v185, v18
	v_max_u32_e32 v23, v32, v23
	v_max_u32_e32 v20, v192, v20
	v_max_u32_e32 v22, v191, v22
	v_max_u32_e32 v18, v185, v18
	v_min_u32_e32 v2, v8, v2
	v_max_u32_e32 v8, v12, v16
	v_min_u32_e32 v12, v12, v16
	v_max_u32_e32 v16, v15, v14
	v_min_u32_e32 v14, v15, v14
	v_max_u32_e32 v15, v10, v11
	v_min_u32_e32 v10, v10, v11
	v_max_u32_e32 v11, v13, v17
	v_min_u32_e32 v13, v13, v17
	v_max_u32_e32 v17, v66, v5
	v_min_u32_e32 v5, v66, v5
	v_max_u32_e32 v66, v7, v9
	v_min_u32_e32 v197, v30, v25
	v_max_u32_e32 v25, v30, v25
	v_min_u32_e32 v196, v29, v21
	v_max_u32_e32 v21, v29, v21
	v_min_u32_e32 v195, v31, v26
	v_min_u32_e32 v193, v24, v19
	v_max_u32_e32 v26, v31, v26
	v_max_u32_e32 v19, v24, v19
	v_min_u32_e32 v31, v23, v20
	v_min_u32_e32 v32, v22, v18
	v_max_u32_e32 v20, v23, v20
	v_max_u32_e32 v18, v22, v18
	v_min_u32_e32 v7, v7, v9
	v_max_u32_e32 v9, v6, v4
	v_min_u32_e32 v4, v6, v4
	v_max_u32_e32 v6, v3, v2
	v_min_u32_e32 v2, v3, v2
	v_min_u32_e32 v3, v8, v16
	v_min_u32_e32 v175, v17, v66
	v_min_u32_e32 v201, v203, v197
	v_min_u32_e32 v30, v28, v25
	v_min_u32_e32 v29, v27, v21
	v_min_u32_e32 v194, v195, v193
	v_min_u32_e32 v24, v26, v19
	v_min_u32_e32 v22, v20, v18
	v_min_u32_e32 v70, v12, v14
	v_min_u32_e32 v73, v10, v13
	v_min_u32_e32 v176, v5, v7
	v_min_u32_e32 v177, v9, v6
	v_min_u32_e32 v183, v4, v2
	v_min_u32_e32 v198, v33, v196
	v_min_u32_e32 v185, v31, v32
	v_max3_u32 v8, v8, v16, v201
	v_max3_u32 v3, v3, v203, v197
	v_max3_u32 v12, v12, v14, v30
	v_max3_u32 v10, v10, v13, v29
	v_max3_u32 v16, v17, v66, v194
	v_max3_u32 v17, v175, v195, v193
	v_max3_u32 v5, v5, v7, v24
	v_max3_u32 v2, v4, v2, v22
	ds_read_b128 v[54:57], v165 offset:40960
	v_min_u32_e32 v72, v15, v11
	v_max3_u32 v11, v15, v11, v198
	v_max3_u32 v13, v73, v27, v21
	v_max3_u32 v7, v176, v26, v19
	v_max3_u32 v6, v9, v6, v185
	v_max3_u32 v9, v177, v31, v32
	v_max_u32_e32 v73, v3, v17
	v_min_u32_e32 v175, v3, v17
	v_max_u32_e32 v176, v12, v5
	v_min_u32_e32 v177, v12, v5
	v_max_u32_e32 v198, v10, v2
	v_min_u32_e32 v199, v10, v2
	ds_read_b128 v[2:5], v161 offset:45056
	v_max3_u32 v14, v70, v28, v25
	v_max3_u32 v15, v72, v33, v196
	v_max3_u32 v66, v183, v20, v18
	v_mfma_f32_32x32x16_bf16 v[18:33], v[42:45], v[34:37], 0
	v_max_u32_e32 v70, v8, v16
	v_max_u32_e32 v183, v14, v7
	v_min_u32_e32 v185, v14, v7
	v_max_u32_e32 v7, v11, v6
	ds_read_b128 v[192:195], v163 offset:40960
	ds_read_b128 v[42:45], v161 offset:49152
	v_min_u32_e32 v72, v8, v16
	v_min_u32_e32 v191, v11, v6
	v_max_u32_e32 v196, v15, v9
	v_min_u32_e32 v197, v15, v9
	v_max_u32_e32 v200, v13, v66
	v_min_u32_e32 v66, v13, v66
	v_max_u32_e32 v201, v70, v7
	v_min_u32_e32 v70, v70, v7
	s_waitcnt lgkmcnt(2)
	v_mfma_f32_32x32x16_bf16 v[2:17], v[2:5], v[34:37], 0
	ds_read_b128 v[34:37], v163 offset:45056
	v_max_u32_e32 v202, v73, v196
	v_min_u32_e32 v73, v73, v196
	v_max_u32_e32 v196, v176, v198
	v_min_u32_e32 v176, v176, v198
	v_max_u32_e32 v198, v183, v200
	v_min_u32_e32 v183, v183, v200
	s_waitcnt lgkmcnt(2)
	v_mfma_f32_32x32x16_bf16 v[18:33], v[192:195], v[38:41], v[18:33]
	v_max_u32_e32 v200, v72, v191
	v_min_u32_e32 v72, v72, v191
	v_max_u32_e32 v191, v175, v197
	v_max_u32_e32 v193, v185, v66
	v_min_u32_e32 v66, v185, v66
	v_max_u32_e32 v185, v201, v196
	v_min_u32_e32 v194, v201, v196
	s_waitcnt lgkmcnt(0)
	v_mfma_f32_32x32x16_bf16 v[2:17], v[34:37], v[38:41], v[2:17]
	ds_read_b128 v[38:41], v165 offset:45056
	v_max_u32_e32 v195, v202, v198
	v_min_u32_e32 v196, v202, v198
	v_max_u32_e32 v198, v191, v193
	v_max_u32_e32 v192, v177, v199
	v_min_u32_e32 v177, v177, v199
	v_min_u32_e32 v175, v175, v197
	v_mfma_f32_32x32x16_bf16 v[18:33], v[54:57], v[62:65], v[18:33]
	ds_read_b128 v[54:57], v167 offset:40960
	ds_read_b128 v[34:37], v165 offset:49152
	v_max_u32_e32 v197, v70, v176
	v_min_u32_e32 v70, v70, v176
	v_max_u32_e32 v176, v73, v183
	v_min_u32_e32 v73, v73, v183
	v_max_u32_e32 v183, v200, v192
	v_min_u32_e32 v192, v200, v192
	s_waitcnt lgkmcnt(2)
	v_mfma_f32_32x32x16_bf16 v[2:17], v[38:41], v[62:65], v[2:17]
	ds_read_b128 v[38:41], v167 offset:45056
	v_min_u32_e32 v62, v191, v193
	v_max_u32_e32 v63, v72, v177
	v_min_u32_e32 v64, v72, v177
	v_min_u32_e32 v72, v185, v195
	v_max_u32_e32 v65, v175, v66
	v_min_u32_e32 v66, v175, v66
	s_waitcnt lgkmcnt(2)
	v_mfma_f32_32x32x16_bf16 v[18:33], v[54:57], v[58:61], v[18:33]
	v_min_u32_e32 v56, v70, v73
	v_min_u32_e32 v57, v183, v198
	v_min_u32_e32 v55, v197, v176
	v_min_u32_e32 v175, v192, v62
	v_min_u32_e32 v177, v63, v65
	v_min_u32_e32 v191, v64, v66
	v_min_u32_e32 v54, v194, v196
	s_waitcnt lgkmcnt(0)
; __device__ __forceinline__ uint32_t mono_key(float f) {
;   uint32_t u = __float_as_uint(f);
;   return (u & 0x80000000u) ? ~u : (u | 0x80000000u);
; }
; __device__ __forceinline__ void bitonic_sort16_desc(uint32_t (&K)[16]) {
; #pragma unroll
;   for (int k = 2; k <= 16; k <<= 1)
; #pragma unroll
;     for (int j = k >> 1; j >= 1; j >>= 1)
; #pragma unroll
;       for (int i = 0; i < 16; ++i) {
;         const int l = i ^ j;
;         if (l > i) { if ((i & k) == 0) ce_desc(K[i], K[l]); else ce_desc(K[l], K[i]); }
;       }
; }
; __device__ void phase_q_route(KParams& p, int bid, int nb, char* smem) {
;     ...
; #pragma unroll
;         for (int i = 0; i < 2; ++i) {
;           uint32_t Kg[16];
; #pragma unroll
;           for (int g2 = 0; g2 < 16; ++g2)
;             Kg[g2] = (mono_key(Sa[i][g2]) & ~0x7Fu) | (uint32_t)((ih * 2 + i) * 32 + (g2 & 3) + 8 * (g2 >> 2)) | kb;
;           bitonic_sort16_desc(Kg);
	v_mfma_f32_32x32x16_bf16 v[2:17], v[38:41], v[58:61], v[2:17]
	s_nop 2
	v_not_b32_e32 v38, v18
	v_or_b32_e32 v39, 0x80000000, v18
	v_cmp_gt_i32_e32 vcc, 0, v18
	v_or_b32_e32 v40, 0x80000000, v21
	v_not_b32_e32 v41, v25
	v_cndmask_b32_e32 v18, v39, v38, vcc
	v_not_b32_e32 v38, v19
	v_or_b32_e32 v39, 0x80000000, v19
	v_cmp_gt_i32_e32 vcc, 0, v19
	v_or_b32_e32 v58, 0x80000000, v25
	v_or_b32_e32 v59, 0x80000000, v22
	v_cndmask_b32_e32 v19, v39, v38, vcc
	v_not_b32_e32 v39, v21
	v_cmp_gt_i32_e32 vcc, 0, v21
	v_not_b32_e32 v61, v33
	v_or_b32_e32 v193, 0x80000000, v33
	v_cndmask_b32_e32 v21, v40, v39, vcc
	v_not_b32_e32 v39, v20
	v_or_b32_e32 v40, 0x80000000, v20
	v_cmp_gt_i32_e32 vcc, 0, v20
	v_or_b32_e32 v199, 0x80000000, v30
	v_not_b32_e32 v200, v26
	v_cndmask_b32_e32 v20, v40, v39, vcc
	v_cmp_gt_i32_e32 vcc, 0, v25
	v_or_b32_e32 v201, 0x80000000, v26
	v_or_b32_e32 v202, 0x80000000, v29
	v_cndmask_b32_e32 v25, v58, v41, vcc
	v_not_b32_e32 v41, v24
	v_or_b32_e32 v58, 0x80000000, v24
	v_cmp_gt_i32_e32 vcc, 0, v24
	v_and_or_b32 v18, v18, s3, v111
	v_and_or_b32 v19, v19, s3, v112
	v_cndmask_b32_e32 v24, v58, v41, vcc
	v_not_b32_e32 v58, v22
	v_cmp_gt_i32_e32 vcc, 0, v22
	v_and_or_b32 v21, v21, s3, v113
	v_and_or_b32 v20, v20, s3, v114
	v_cndmask_b32_e32 v22, v59, v58, vcc
	v_not_b32_e32 v58, v23
	v_or_b32_e32 v59, 0x80000000, v23
	v_cmp_gt_i32_e32 vcc, 0, v23
	v_and_or_b32 v25, v25, s3, v115
	v_and_or_b32 v24, v24, s3, v116
	v_cndmask_b32_e32 v23, v59, v58, vcc
	v_cmp_gt_i32_e32 vcc, 0, v33
	v_and_or_b32 v22, v22, s3, v117
	v_and_or_b32 v23, v23, s3, v118
	v_cndmask_b32_e32 v33, v193, v61, vcc
	v_not_b32_e32 v61, v32
	v_or_b32_e32 v193, 0x80000000, v32
	v_cmp_gt_i32_e32 vcc, 0, v32
	v_and_or_b32 v33, v33, s3, v119
	v_max_u32_e32 v38, v18, v19
	v_cndmask_b32_e32 v32, v193, v61, vcc
	v_not_b32_e32 v193, v30
	v_cmp_gt_i32_e32 vcc, 0, v30
	v_and_or_b32 v32, v32, s3, v120
	v_min_u32_e32 v39, v21, v20
	v_cndmask_b32_e32 v30, v199, v193, vcc
	v_not_b32_e32 v193, v31
	v_or_b32_e32 v199, 0x80000000, v31
	v_cmp_gt_i32_e32 vcc, 0, v31
	v_and_or_b32 v30, v30, s3, v121
	v_min_u32_e32 v18, v18, v19
	v_cndmask_b32_e32 v31, v199, v193, vcc
	v_cmp_gt_i32_e32 vcc, 0, v26
	v_and_or_b32 v31, v31, s3, v122
	v_max_u32_e32 v19, v21, v20
	v_cndmask_b32_e32 v26, v201, v200, vcc
	v_not_b32_e32 v200, v27
	v_or_b32_e32 v201, 0x80000000, v27
	v_cmp_gt_i32_e32 vcc, 0, v27
	v_and_or_b32 v26, v26, s3, v123
	v_max_u32_e32 v41, v25, v24
	v_cndmask_b32_e32 v27, v201, v200, vcc
	v_not_b32_e32 v201, v29
	v_cmp_gt_i32_e32 vcc, 0, v29
	v_and_or_b32 v27, v27, s3, v124
	v_min_u32_e32 v58, v22, v23
	v_cndmask_b32_e32 v29, v202, v201, vcc
	v_not_b32_e32 v201, v28
	v_or_b32_e32 v202, 0x80000000, v28
	v_cmp_gt_i32_e32 vcc, 0, v28
	v_and_or_b32 v29, v29, s3, v125
	v_min_u32_e32 v24, v25, v24
	v_cndmask_b32_e32 v28, v202, v201, vcc
	v_and_or_b32 v28, v28, s3, v126
	v_max_u32_e32 v22, v22, v23
	v_max_u32_e32 v61, v33, v32
	v_min_u32_e32 v193, v30, v31
	v_min_u32_e32 v32, v33, v32
	v_max_u32_e32 v30, v30, v31
	v_max_u32_e32 v200, v26, v27
	v_min_u32_e32 v201, v29, v28
	v_min_u32_e32 v26, v26, v27
	v_max_u32_e32 v27, v29, v28
	v_max_u32_e32 v40, v38, v39
	v_max_u32_e32 v20, v18, v19
	v_min_u32_e32 v59, v41, v58
	v_min_u32_e32 v23, v24, v22
	v_min_u32_e32 v38, v38, v39
	v_min_u32_e32 v18, v18, v19
	v_max_u32_e32 v39, v41, v58
	v_max_u32_e32 v22, v24, v22
	v_max_u32_e32 v199, v61, v193
	v_max_u32_e32 v31, v32, v30
	v_min_u32_e32 v202, v200, v201
	v_min_u32_e32 v28, v26, v27
	v_min_u32_e32 v61, v61, v193
	v_min_u32_e32 v30, v32, v30
	v_max_u32_e32 v193, v200, v201
	v_max_u32_e32 v26, v26, v27
	v_max_u32_e32 v21, v40, v20
	v_min_u32_e32 v25, v59, v23
	v_max_u32_e32 v19, v38, v18
	v_min_u32_e32 v24, v39, v22
	v_min_u32_e32 v20, v40, v20
	v_max_u32_e32 v23, v59, v23
	v_min_u32_e32 v18, v38, v18
	v_max_u32_e32 v22, v39, v22
	v_max_u32_e32 v33, v199, v31
	v_min_u32_e32 v29, v202, v28
	v_max_u32_e32 v32, v61, v30
	v_min_u32_e32 v27, v193, v26
	v_min_u32_e32 v31, v199, v31
	v_max_u32_e32 v28, v202, v28
	v_min_u32_e32 v30, v61, v30
	v_max_u32_e32 v26, v193, v26
	v_max_u32_e32 v60, v21, v25
	v_max_u32_e32 v41, v19, v24
	v_max_u32_e32 v40, v20, v23
	v_max_u32_e32 v38, v18, v22
	v_min_u32_e32 v203, v33, v29
	v_min_u32_e32 v200, v32, v27
	v_min_u32_e32 v199, v31, v28
	v_min_u32_e32 v61, v30, v26
	v_min_u32_e32 v21, v21, v25
	v_min_u32_e32 v19, v19, v24
	v_min_u32_e32 v20, v20, v23
	v_min_u32_e32 v18, v18, v22
	v_max_u32_e32 v25, v33, v29
	v_max_u32_e32 v27, v32, v27
	v_max_u32_e32 v28, v31, v28
	v_max_u32_e32 v26, v30, v26
	v_max_u32_e32 v58, v60, v41
	v_max_u32_e32 v39, v40, v38
	v_min_u32_e32 v201, v203, v200
	v_min_u32_e32 v193, v199, v61
	v_max_u32_e32 v24, v21, v19
	v_max_u32_e32 v22, v20, v18
	v_min_u32_e32 v29, v25, v27
	v_min_u32_e32 v30, v28, v26
	v_min_u32_e32 v41, v60, v41
	v_min_u32_e32 v38, v40, v38
	v_max_u32_e32 v60, v203, v200
	v_max_u32_e32 v61, v199, v61
	v_min_u32_e32 v19, v21, v19
	v_min_u32_e32 v18, v20, v18
	v_max_u32_e32 v21, v25, v27
	v_max_u32_e32 v25, v28, v26
	v_max_u32_e32 v59, v58, v39
	v_min_u32_e32 v202, v201, v193
	v_max_u32_e32 v23, v24, v22
	v_min_u32_e32 v31, v29, v30
	v_max_u32_e32 v40, v41, v38
	v_min_u32_e32 v199, v60, v61
	v_max_u32_e32 v20, v19, v18
	v_min_u32_e32 v26, v21, v25
	v_min_u32_e32 v204, v59, v202
	v_min_u32_e32 v32, v23, v31
	v_min_u32_e32 v200, v40, v199
	v_min_u32_e32 v27, v20, v26
	v_min_u32_e32 v33, v204, v32
	v_min_u32_e32 v28, v200, v27
	v_min_u32_e32 v39, v58, v39
	v_max_u32_e32 v58, v201, v193
	v_min_u32_e32 v22, v24, v22
	v_max_u32_e32 v24, v29, v30
	v_min_u32_e32 v38, v41, v38
	v_max_u32_e32 v41, v60, v61
	v_min_u32_e32 v18, v19, v18
; __device__ __forceinline__ void bitonic_sort16_desc(uint32_t (&K)[16]) {
; #pragma unroll
;   for (int k = 2; k <= 16; k <<= 1)
; #pragma unroll
;     for (int j = k >> 1; j >= 1; j >>= 1)
; #pragma unroll
;       for (int i = 0; i < 16; ++i) {
;         const int l = i ^ j;
;         if (l > i) { if ((i & k) == 0) ce_desc(K[i], K[l]); else ce_desc(K[l], K[i]); }
;       }
; }
; __device__ __forceinline__ void merge_top16(uint32_t (&Lk)[16], const uint32_t (&K)[16]) {
; #pragma unroll
;   for (int i = 0; i < 16; ++i) Lk[i] = max(Lk[i], K[15 - i]);
; #pragma unroll
;   for (int dd = 8; dd >= 1; dd >>= 1)
; #pragma unroll
;     for (int i = 0; i < 16; ++i)
;       if ((i & dd) == 0) ce_desc(Lk[i], Lk[i + dd]);
; }
; __device__ void phase_q_route(KParams& p, int bid, int nb, char* smem) {
;     ...
;             Kg[g2] = (mono_key(Sa[i][g2]) & ~0x7Fu) | (uint32_t)((ih * 2 + i) * 32 + (g2 & 3) + 8 * (g2 >> 2)) | kb;
	v_max_u32_e32 v19, v21, v25
	v_max_u32_e32 v32, v204, v32
	v_max_u32_e32 v27, v200, v27
	v_min_u32_e32 v203, v33, v28
	v_min_u32_e32 v193, v39, v58
	v_min_u32_e32 v29, v22, v24
	v_min_u32_e32 v60, v38, v41
	v_min_u32_e32 v21, v18, v19
	v_max_u32_e32 v28, v33, v28
	v_min_u32_e32 v33, v32, v27
	v_max_u32_e32 v27, v32, v27
	v_max_u32_e32 v32, v59, v202
	v_max_u32_e32 v23, v23, v31
	v_max_u32_e32 v40, v40, v199
	v_max_u32_e32 v20, v20, v26
	v_max_u32_e32 v39, v39, v58
	v_max_u32_e32 v22, v22, v24
	v_max_u32_e32 v38, v38, v41
	v_max_u32_e32 v18, v18, v19
	v_min_u32_e32 v31, v32, v23
	v_min_u32_e32 v26, v40, v20
	v_min_u32_e32 v24, v39, v22
	v_min_u32_e32 v19, v38, v18
	v_min_u32_e32 v30, v193, v29
	v_min_u32_e32 v25, v60, v21
	v_max_u32_e32 v29, v193, v29
	v_max_u32_e32 v21, v60, v21
	v_min_u32_e32 v59, v31, v26
	v_min_u32_e32 v41, v24, v19
	v_min_u32_e32 v60, v29, v21
	v_max_u32_e32 v21, v29, v21
	v_min_u32_e32 v58, v59, v41
	v_min_u32_e32 v29, v27, v21
	v_max_u32_e32 v20, v40, v20
	v_max3_u32 v21, v56, v27, v21
	v_max3_u32 v27, v183, v198, v58
	v_max3_u32 v40, v57, v59, v41
	v_not_b32_e32 v58, v2
	v_or_b32_e32 v59, 0x80000000, v2
	v_cmp_gt_i32_e32 vcc, 0, v2
	v_min_u32_e32 v193, v33, v60
	v_max_u32_e32 v26, v31, v26
	v_cndmask_b32_e32 v2, v59, v58, vcc
	v_not_b32_e32 v58, v3
	v_or_b32_e32 v59, 0x80000000, v3
	v_cmp_gt_i32_e32 vcc, 0, v3
	v_max_u32_e32 v19, v24, v19
	v_max3_u32 v33, v55, v33, v60
	v_cndmask_b32_e32 v3, v59, v58, vcc
	v_not_b32_e32 v59, v5
	v_or_b32_e32 v60, 0x80000000, v5
	v_cmp_gt_i32_e32 vcc, 0, v5
	v_min_u32_e32 v61, v30, v25
	v_min_u32_e32 v24, v26, v19
	v_max_u32_e32 v23, v32, v23
	v_max_u32_e32 v22, v39, v22
	v_max_u32_e32 v18, v38, v18
	v_cndmask_b32_e32 v5, v60, v59, vcc
	v_not_b32_e32 v59, v4
	v_or_b32_e32 v60, 0x80000000, v4
	v_cmp_gt_i32_e32 vcc, 0, v4
	v_min_u32_e32 v201, v203, v61
	v_min_u32_e32 v31, v23, v20
	v_min_u32_e32 v32, v22, v18
	v_max3_u32 v39, v72, v203, v61
	v_max3_u32 v24, v192, v62, v24
	v_cndmask_b32_e32 v4, v60, v59, vcc
	v_not_b32_e32 v61, v9
	v_or_b32_e32 v62, 0x80000000, v9
	v_cmp_gt_i32_e32 vcc, 0, v9
	v_min_u32_e32 v38, v31, v32
	v_max_u32_e32 v20, v23, v20
	v_cndmask_b32_e32 v9, v62, v61, vcc
	v_not_b32_e32 v61, v8
	v_or_b32_e32 v62, 0x80000000, v8
	v_cmp_gt_i32_e32 vcc, 0, v8
	v_max_u32_e32 v18, v22, v18
	v_max3_u32 v19, v175, v26, v19
	v_max3_u32 v26, v63, v65, v38
	v_cndmask_b32_e32 v8, v62, v61, vcc
	v_not_b32_e32 v62, v6
	v_or_b32_e32 v63, 0x80000000, v6
	v_cmp_gt_i32_e32 vcc, 0, v6
	v_min_u32_e32 v22, v20, v18
	v_max3_u32 v22, v64, v66, v22
	v_cndmask_b32_e32 v6, v63, v62, vcc
	v_not_b32_e32 v62, v7
	v_or_b32_e32 v63, 0x80000000, v7
	v_cmp_gt_i32_e32 vcc, 0, v7
	v_not_b32_e32 v65, v17
	v_or_b32_e32 v66, 0x80000000, v17
	v_cndmask_b32_e32 v7, v63, v62, vcc
	v_cmp_gt_i32_e32 vcc, 0, v17
	v_max3_u32 v29, v70, v73, v29
	v_or_b32_e32 v70, 0x80000000, v14
	v_cndmask_b32_e32 v17, v66, v65, vcc
	v_not_b32_e32 v65, v16
	v_or_b32_e32 v66, 0x80000000, v16
	v_cmp_gt_i32_e32 vcc, 0, v16
	v_not_b32_e32 v72, v10
	v_or_b32_e32 v73, 0x80000000, v10
	v_cndmask_b32_e32 v16, v66, v65, vcc
	v_not_b32_e32 v66, v14
	v_cmp_gt_i32_e32 vcc, 0, v14
	v_or_b32_e32 v175, 0x80000000, v13
	v_and_or_b32 v2, v2, s3, v127
	v_cndmask_b32_e32 v14, v70, v66, vcc
	v_not_b32_e32 v66, v15
	v_or_b32_e32 v70, 0x80000000, v15
	v_cmp_gt_i32_e32 vcc, 0, v15
	v_and_or_b32 v3, v3, s3, v128
	v_and_or_b32 v5, v5, s3, v129
	v_cndmask_b32_e32 v15, v70, v66, vcc
	v_cmp_gt_i32_e32 vcc, 0, v10
	v_and_or_b32 v4, v4, s3, v130
	v_and_or_b32 v9, v9, s3, v131
	v_cndmask_b32_e32 v10, v73, v72, vcc
	v_not_b32_e32 v72, v11
	v_or_b32_e32 v73, 0x80000000, v11
	v_cmp_gt_i32_e32 vcc, 0, v11
	v_and_or_b32 v8, v8, s3, v132
	v_and_or_b32 v6, v6, s3, v133
	v_cndmask_b32_e32 v11, v73, v72, vcc
	v_not_b32_e32 v73, v13
	v_cmp_gt_i32_e32 vcc, 0, v13
	v_and_or_b32 v7, v7, s3, v134
	v_and_or_b32 v17, v17, s3, v135
	v_cndmask_b32_e32 v13, v175, v73, vcc
	v_not_b32_e32 v73, v12
	v_or_b32_e32 v175, 0x80000000, v12
	v_cmp_gt_i32_e32 vcc, 0, v12
	v_and_or_b32 v16, v16, s3, v136
	v_and_or_b32 v14, v14, s3, v137
	v_cndmask_b32_e32 v12, v175, v73, vcc
	v_and_or_b32 v15, v15, s3, v138
	v_and_or_b32 v10, v10, s3, v139
	v_and_or_b32 v11, v11, s3, v140
	v_and_or_b32 v13, v13, s3, v141
	v_and_or_b32 v12, v12, s3, v142
	v_max_u32_e32 v58, v2, v3
	v_min_u32_e32 v59, v5, v4
	v_min_u32_e32 v2, v2, v3
	v_max_u32_e32 v3, v5, v4
	v_max_u32_e32 v61, v9, v8
	v_min_u32_e32 v62, v6, v7
	v_min_u32_e32 v8, v9, v8
	v_max_u32_e32 v6, v6, v7
	v_max_u32_e32 v65, v17, v16
	v_min_u32_e32 v66, v14, v15
	v_min_u32_e32 v16, v17, v16
	v_max_u32_e32 v14, v14, v15
	v_max_u32_e32 v72, v10, v11
	v_min_u32_e32 v73, v13, v12
	v_min_u32_e32 v10, v10, v11
	v_max_u32_e32 v11, v13, v12
	v_max_u32_e32 v60, v58, v59
	v_max_u32_e32 v4, v2, v3
	v_min_u32_e32 v63, v61, v62
	v_min_u32_e32 v7, v8, v6
	v_min_u32_e32 v58, v58, v59
	v_min_u32_e32 v2, v2, v3
	v_max_u32_e32 v59, v61, v62
	v_max_u32_e32 v6, v8, v6
	v_max_u32_e32 v70, v65, v66
	v_max_u32_e32 v15, v16, v14
	v_min_u32_e32 v175, v72, v73
	v_min_u32_e32 v12, v10, v11
	v_min_u32_e32 v65, v65, v66
	v_min_u32_e32 v14, v16, v14
	v_max_u32_e32 v66, v72, v73
	v_max_u32_e32 v10, v10, v11
	v_max_u32_e32 v25, v30, v25
	v_max_u32_e32 v5, v60, v4
	v_min_u32_e32 v9, v63, v7
	v_max_u32_e32 v3, v58, v2
	v_min_u32_e32 v8, v59, v6
	v_min_u32_e32 v4, v60, v4
	v_max_u32_e32 v7, v63, v7
	v_min_u32_e32 v2, v58, v2
	v_max_u32_e32 v6, v59, v6
	v_max_u32_e32 v17, v70, v15
	v_min_u32_e32 v13, v175, v12
	v_max_u32_e32 v16, v65, v14
	v_min_u32_e32 v11, v66, v10
	v_min_u32_e32 v15, v70, v15
	v_max_u32_e32 v12, v175, v12
	v_min_u32_e32 v14, v65, v14
	v_max_u32_e32 v10, v66, v10
; __device__ __forceinline__ void bitonic_sort16_desc(uint32_t (&K)[16]) {
; #pragma unroll
;   for (int k = 2; k <= 16; k <<= 1)
; #pragma unroll
;     for (int j = k >> 1; j >= 1; j >>= 1)
; #pragma unroll
;       for (int i = 0; i < 16; ++i) {
;         const int l = i ^ j;
;         if (l > i) { if ((i & k) == 0) ce_desc(K[i], K[l]); else ce_desc(K[l], K[i]); }
;       }
; }
; __device__ __forceinline__ void merge_top16(uint32_t (&Lk)[16], const uint32_t (&K)[16]) {
; #pragma unroll
;   for (int i = 0; i < 16; ++i) Lk[i] = max(Lk[i], K[15 - i]);
; #pragma unroll
;   for (int dd = 8; dd >= 1; dd >>= 1)
; #pragma unroll
;     for (int i = 0; i < 16; ++i)
;       if ((i & dd) == 0) ce_desc(Lk[i], Lk[i + dd]);
; }
	v_min_u32_e32 v30, v28, v25
	v_max3_u32 v25, v54, v28, v25
	v_max3_u32 v28, v197, v176, v193
	v_max_u32_e32 v64, v5, v9
	v_max_u32_e32 v61, v3, v8
	v_max_u32_e32 v60, v4, v7
	v_max_u32_e32 v58, v2, v6
	v_min_u32_e32 v176, v17, v13
	v_min_u32_e32 v72, v16, v11
	v_min_u32_e32 v70, v15, v12
	v_min_u32_e32 v65, v14, v10
	v_min_u32_e32 v5, v5, v9
	v_min_u32_e32 v3, v3, v8
	v_min_u32_e32 v4, v4, v7
	v_min_u32_e32 v2, v2, v6
	v_max_u32_e32 v9, v17, v13
	v_max_u32_e32 v11, v16, v11
	v_max_u32_e32 v12, v15, v12
	v_max_u32_e32 v10, v14, v10
	v_max_u32_e32 v62, v64, v61
	v_max_u32_e32 v59, v60, v58
	v_min_u32_e32 v73, v176, v72
	v_min_u32_e32 v66, v70, v65
	v_max_u32_e32 v8, v5, v3
	v_max_u32_e32 v6, v4, v2
	v_min_u32_e32 v13, v9, v11
	v_min_u32_e32 v14, v12, v10
	v_min_u32_e32 v61, v64, v61
	v_min_u32_e32 v58, v60, v58
	v_max_u32_e32 v64, v176, v72
	v_max_u32_e32 v65, v70, v65
	v_min_u32_e32 v3, v5, v3
	v_min_u32_e32 v2, v4, v2
	v_max_u32_e32 v5, v9, v11
	v_max_u32_e32 v9, v12, v10
	v_max_u32_e32 v63, v62, v59
	v_min_u32_e32 v175, v73, v66
	v_max_u32_e32 v7, v8, v6
	v_min_u32_e32 v15, v13, v14
	v_max_u32_e32 v60, v61, v58
	v_min_u32_e32 v70, v64, v65
	v_max_u32_e32 v4, v3, v2
	v_min_u32_e32 v10, v5, v9
	v_min_u32_e32 v59, v62, v59
	v_max_u32_e32 v62, v73, v66
	v_min_u32_e32 v6, v8, v6
	v_max_u32_e32 v8, v13, v14
	v_min_u32_e32 v58, v61, v58
	v_max_u32_e32 v61, v64, v65
	v_min_u32_e32 v2, v3, v2
	v_max_u32_e32 v3, v5, v9
	v_max3_u32 v23, v185, v195, v201
	v_max3_u32 v30, v194, v196, v30
	v_max3_u32 v31, v177, v31, v32
	v_max3_u32 v18, v191, v20, v18
	v_min_u32_e32 v177, v63, v175
	v_min_u32_e32 v16, v7, v15
	v_min_u32_e32 v72, v60, v70
	v_min_u32_e32 v11, v4, v10
	v_min_u32_e32 v66, v59, v62
	v_min_u32_e32 v13, v6, v8
	v_min_u32_e32 v64, v58, v61
	v_min_u32_e32 v5, v2, v3
	v_max_u32_e32 v20, v23, v27
	v_min_u32_e32 v23, v23, v27
	v_max_u32_e32 v27, v39, v40
	v_max_u32_e32 v38, v30, v24
	v_min_u32_e32 v24, v30, v24
	v_max_u32_e32 v30, v25, v19
	v_min_u32_e32 v19, v25, v19
	v_max_u32_e32 v25, v28, v26
	v_min_u32_e32 v26, v28, v26
	v_max_u32_e32 v28, v33, v31
	v_min_u32_e32 v31, v33, v31
	v_max_u32_e32 v33, v29, v22
	v_min_u32_e32 v22, v29, v22
	v_max_u32_e32 v29, v21, v18
	v_min_u32_e32 v17, v177, v16
	v_min_u32_e32 v12, v72, v11
	v_min_u32_e32 v14, v66, v13
	v_min_u32_e32 v9, v64, v5
	v_min_u32_e32 v32, v39, v40
	v_min_u32_e32 v18, v21, v18
	v_max_u32_e32 v21, v20, v25
	v_min_u32_e32 v20, v20, v25
	v_max_u32_e32 v25, v27, v28
	v_min_u32_e32 v27, v27, v28
	v_max_u32_e32 v28, v38, v33
	v_min_u32_e32 v33, v38, v33
	v_max_u32_e32 v38, v30, v29
	v_min_u32_e32 v176, v17, v12
	v_min_u32_e32 v65, v14, v9
	v_min_u32_e32 v29, v30, v29
	v_max_u32_e32 v30, v23, v26
	v_min_u32_e32 v23, v23, v26
	v_max_u32_e32 v26, v32, v31
	v_min_u32_e32 v31, v32, v31
	v_max_u32_e32 v32, v24, v22
	v_min_u32_e32 v22, v24, v22
	v_max_u32_e32 v24, v19, v18
	v_min_u32_e32 v18, v19, v18
	v_max_u32_e32 v19, v21, v28
	v_min_u32_e32 v21, v21, v28
	v_max_u32_e32 v28, v25, v38
	v_min_u32_e32 v73, v176, v65
	v_min_u32_e32 v25, v25, v38
	v_max_u32_e32 v38, v20, v33
	v_min_u32_e32 v20, v20, v33
	v_max_u32_e32 v33, v27, v29
	v_min_u32_e32 v27, v27, v29
	v_max_u32_e32 v29, v30, v32
	v_min_u32_e32 v30, v30, v32
	v_max_u32_e32 v32, v26, v24
	v_min_u32_e32 v24, v26, v24
	v_max_u32_e32 v26, v23, v22
	v_min_u32_e32 v22, v23, v22
	v_max_u32_e32 v23, v31, v18
	v_min_u32_e32 v18, v31, v18
	v_min_u32_e32 v31, v19, v28
	v_max3_u32 v19, v19, v28, v73
	v_max_u32_e32 v28, v63, v175
	v_max_u32_e32 v7, v7, v15
	v_max_u32_e32 v60, v60, v70
	v_max_u32_e32 v4, v4, v10
	v_max_u32_e32 v59, v59, v62
	v_max_u32_e32 v6, v6, v8
	v_max_u32_e32 v58, v58, v61
	v_max_u32_e32 v2, v2, v3
	v_min_u32_e32 v15, v28, v7
	v_min_u32_e32 v10, v60, v4
	v_min_u32_e32 v8, v59, v6
	v_min_u32_e32 v3, v58, v2
	v_min_u32_e32 v63, v15, v10
	v_min_u32_e32 v61, v8, v3
	v_min_u32_e32 v62, v63, v61
	v_max_u32_e32 v16, v177, v16
	v_max_u32_e32 v11, v72, v11
	v_max_u32_e32 v13, v66, v13
	v_max_u32_e32 v5, v64, v5
	v_min_u32_e32 v54, v29, v32
	v_max3_u32 v29, v29, v32, v62
	v_min_u32_e32 v62, v16, v11
	v_min_u32_e32 v64, v13, v5
	v_min_u32_e32 v66, v62, v64
	v_max_u32_e32 v7, v28, v7
	v_max_u32_e32 v4, v60, v4
	v_max_u32_e32 v6, v59, v6
	v_max_u32_e32 v2, v58, v2
	v_min_u32_e32 v40, v38, v33
	v_max3_u32 v33, v38, v33, v66
	v_min_u32_e32 v28, v7, v4
	v_min_u32_e32 v38, v6, v2
	v_max_u32_e32 v12, v17, v12
	v_max_u32_e32 v9, v14, v9
	v_max_u32_e32 v10, v15, v10
	v_max_u32_e32 v3, v8, v3
	v_max_u32_e32 v11, v16, v11
	v_max_u32_e32 v5, v13, v5
	v_max_u32_e32 v4, v7, v4
	v_max_u32_e32 v2, v6, v2
	v_min_u32_e32 v39, v21, v25
	v_min_u32_e32 v41, v20, v27
	v_min_u32_e32 v55, v30, v24
	v_min_u32_e32 v56, v26, v23
	v_min_u32_e32 v57, v22, v18
	v_min_u32_e32 v58, v28, v38
	v_min_u32_e32 v14, v12, v9
	v_min_u32_e32 v8, v10, v3
	v_min_u32_e32 v13, v11, v5
	v_min_u32_e32 v6, v4, v2
	v_max3_u32 v23, v26, v23, v58
	v_max3_u32 v14, v21, v25, v14
	v_max3_u32 v8, v30, v24, v8
	v_max3_u32 v13, v20, v27, v13
	v_max3_u32 v6, v22, v18, v6
	v_max3_u32 v18, v31, v176, v65
	v_max3_u32 v20, v54, v63, v61
	v_max3_u32 v22, v40, v62, v64
	v_max3_u32 v24, v56, v28, v38
	v_max3_u32 v9, v39, v12, v9
	v_max3_u32 v3, v55, v10, v3
	v_max3_u32 v5, v41, v11, v5
	v_max3_u32 v2, v57, v4, v2
	v_min_u32_e32 v32, v19, v29
	v_min_u32_e32 v26, v33, v23
	v_min_u32_e32 v15, v14, v8
	v_min_u32_e32 v7, v13, v6
	v_min_u32_e32 v21, v18, v20
	v_min_u32_e32 v25, v22, v24
	v_min_u32_e32 v10, v9, v3
	v_min_u32_e32 v4, v5, v2
	v_min_u32_e32 v58, v32, v26
	v_min_u32_e32 v16, v15, v7
	v_min_u32_e32 v27, v21, v25
	v_min_u32_e32 v11, v10, v4
	v_min_u32_e32 v17, v58, v16
	v_min_u32_e32 v12, v27, v11
; __device__ void phase_q_route(KParams& p, int bid, int nb, char* smem) {
;     ...
;         for (int ks = 0; ks < 4; ++ks) {
;           const bf16x8 qb = *reinterpret_cast<const bf16x8*>(smem + swz16(w * 32 + l31, sd * 8 + ks * 2 + lh));
; #pragma unroll
;           for (int i = 0; i < 2; ++i) {
;             const bf16x8 ka = *reinterpret_cast<const bf16x8*>(smem + 32768 + swz8(sd * 128 + (ih * 2 + i) * 32 + l31, ks * 2 + lh));
;             Sa[i] = __builtin_amdgcn_mfma_f32_32x32x16_bf16(ka, qb, Sa[i], 0, 0, 0);
;           }
;     ...
; #pragma unroll
;       for (int i = 0; i < 8; ++i) {
;         const uint32_t t1 = (uint32_t)__shfl_xor((int)Lk[15 - i], 32), t2 = (uint32_t)__shfl_xor((int)Lk[i], 32);
;         Lk[i] = max(Lk[i], t1); Lk[15 - i] = max(Lk[15 - i], t2);
;       }
; #pragma unroll
;       for (int dd = 8; dd >= 1; dd >>= 1)
; #pragma unroll
;         for (int i = 0; i < 16; ++i)
;           if ((i & dd) == 0) { const uint32_t hi = max(Lk[i], Lk[i + dd]), lo = min(Lk[i], Lk[i + dd]); Lk[i] = hi; Lk[i + dd] = lo; }
	v_max_u32_e32 v16, v58, v16
	v_max_u32_e32 v11, v27, v11
	v_min_u32_e32 v28, v17, v12
	v_max_u32_e32 v12, v17, v12
	v_min_u32_e32 v17, v16, v11
	v_max_u32_e32 v11, v16, v11
	v_max_u32_e32 v16, v32, v26
	v_max_u32_e32 v7, v15, v7
	v_max_u32_e32 v21, v21, v25
	v_max_u32_e32 v4, v10, v4
	v_min_u32_e32 v15, v16, v7
	v_min_u32_e32 v10, v21, v4
	v_max_u32_e32 v7, v16, v7
	v_max_u32_e32 v4, v21, v4
	v_min_u32_e32 v38, v15, v10
	v_max_u32_e32 v66, v15, v10
	v_min_u32_e32 v70, v7, v4
	v_max_u32_e32 v198, v7, v4
	v_max_u32_e32 v4, v19, v29
	v_max_u32_e32 v7, v33, v23
	v_max_u32_e32 v8, v14, v8
	v_max_u32_e32 v6, v13, v6
	v_max_u32_e32 v15, v18, v20
	v_max_u32_e32 v16, v22, v24
	v_max_u32_e32 v3, v9, v3
	v_max_u32_e32 v2, v5, v2
	v_min_u32_e32 v10, v4, v7
	v_min_u32_e32 v13, v8, v6
	v_min_u32_e32 v18, v15, v16
	v_min_u32_e32 v5, v3, v2
	v_min_u32_e32 v14, v10, v13
	v_min_u32_e32 v9, v18, v5
	v_min_u32_e32 v196, v14, v9
	v_max_u32_e32 v195, v14, v9
	v_max_u32_e32 v9, v10, v13
	v_max_u32_e32 v5, v18, v5
	v_min_u32_e32 v193, v9, v5
	v_max_u32_e32 v9, v9, v5
	v_max_u32_e32 v4, v4, v7
	v_max_u32_e32 v5, v8, v6
	v_max_u32_e32 v7, v15, v16
	v_max_u32_e32 v2, v3, v2
	v_min_u32_e32 v6, v4, v5
	v_min_u32_e32 v3, v7, v2
	v_max_u32_e32 v4, v4, v5
	v_max_u32_e32 v2, v7, v2
	v_max_u32_e32 v199, v4, v2
	ds_bpermute_b32 v5, v71, v199
	v_min_u32_e32 v2, v4, v2
	ds_bpermute_b32 v4, v71, v12
	v_min_u32_e32 v8, v6, v3
	v_max_u32_e32 v3, v6, v3
	s_waitcnt lgkmcnt(1)
	v_max_u32_e32 v72, v28, v5
	ds_bpermute_b32 v5, v71, v2
	ds_bpermute_b32 v6, v71, v17
	s_waitcnt lgkmcnt(2)
	v_max_u32_e32 v175, v2, v4
	ds_bpermute_b32 v2, v71, v11
	ds_read_b128 v[58:61], v168
	ds_bpermute_b32 v7, v71, v3
	ds_bpermute_b32 v200, v71, v28
	s_waitcnt lgkmcnt(4)
	v_max_u32_e32 v177, v3, v6
	ds_bpermute_b32 v6, v71, v8
	s_waitcnt lgkmcnt(4)
	v_max_u32_e32 v183, v8, v2
	ds_bpermute_b32 v8, v71, v9
	s_waitcnt lgkmcnt(4)
	v_mfma_f32_32x32x16_bf16 v[18:33], v[42:45], v[58:61], 0
	ds_bpermute_b32 v42, v71, v66
	ds_bpermute_b32 v43, v71, v193
	s_waitcnt lgkmcnt(5)
	v_max_u32_e32 v176, v17, v7
	ds_bpermute_b32 v7, v71, v38
	v_max_u32_e32 v73, v12, v5
	ds_read_b128 v[2:5], v161 offset:53248
	ds_read_b128 v[54:57], v169
	s_waitcnt lgkmcnt(5)
	v_max_u32_e32 v192, v38, v8
	ds_read_b128 v[38:41], v163 offset:49152
	ds_read_b128 v[62:65], v161 offset:57344
	s_waitcnt lgkmcnt(6)
	v_max_u32_e32 v193, v193, v42
	s_waitcnt lgkmcnt(5)
	v_max_u32_e32 v194, v66, v43
	ds_read_b128 v[42:45], v163 offset:53248
	v_max_u32_e32 v185, v11, v6
	s_waitcnt lgkmcnt(5)
	v_max_u32_e32 v191, v9, v7
	s_waitcnt lgkmcnt(4)
	v_mfma_f32_32x32x16_bf16 v[2:17], v[2:5], v[58:61], 0
	ds_bpermute_b32 v202, v71, v196
	ds_bpermute_b32 v201, v71, v198
	ds_bpermute_b32 v66, v71, v70
	ds_bpermute_b32 v197, v71, v195
	v_max_u32_e32 v207, v193, v176
	s_waitcnt lgkmcnt(3)
	v_max_u32_e32 v198, v198, v202
	s_waitcnt lgkmcnt(2)
	v_max_u32_e32 v196, v196, v201
	v_mfma_f32_32x32x16_bf16 v[18:33], v[38:41], v[54:57], v[18:33]
	s_waitcnt lgkmcnt(1)
	v_max_u32_e32 v195, v195, v66
	s_waitcnt lgkmcnt(0)
	v_max_u32_e32 v197, v70, v197
	v_max_u32_e32 v201, v199, v200
	v_max_u32_e32 v66, v201, v198
	v_max_u32_e32 v70, v175, v197
	v_max_u32_e32 v200, v177, v194
	v_max_u32_e32 v199, v191, v185
	v_mfma_f32_32x32x16_bf16 v[2:17], v[42:45], v[54:57], v[2:17]
	ds_read_b128 v[42:45], v170
	ds_read_b128 v[202:205], v165 offset:53248
	ds_read_b128 v[38:41], v171
	v_max_u32_e32 v208, v195, v73
	v_max_u32_e32 v218, v66, v199
	v_min_u32_e32 v199, v66, v199
	v_max_u32_e32 v66, v70, v207
	v_max_u32_e32 v206, v183, v192
	s_waitcnt lgkmcnt(2)
	v_mfma_f32_32x32x16_bf16 v[18:33], v[34:37], v[42:45], v[18:33]
	ds_read_b128 v[210:213], v167 offset:49152
	ds_read_b128 v[34:37], v165 offset:57344
	ds_read_b128 v[214:217], v167 offset:53248
	v_max_u32_e32 v209, v196, v72
	s_waitcnt lgkmcnt(2)
	v_mfma_f32_32x32x16_bf16 v[18:33], v[210:213], v[38:41], v[18:33]
	v_mfma_f32_32x32x16_bf16 v[2:17], v[202:205], v[42:45], v[2:17]
	s_nop 10
	v_not_b32_e32 v210, v18
	v_or_b32_e32 v211, 0x80000000, v18
	v_cmp_gt_i32_e32 vcc, 0, v18
	v_min_u32_e32 v205, v70, v207
	v_max_u32_e32 v70, v200, v208
	v_cndmask_b32_e32 v18, v211, v210, vcc
	v_not_b32_e32 v210, v19
	v_or_b32_e32 v211, 0x80000000, v19
	v_cmp_gt_i32_e32 vcc, 0, v19
	s_waitcnt lgkmcnt(0)
; __device__ __forceinline__ uint32_t mono_key(float f) {
;   uint32_t u = __float_as_uint(f);
;   return (u & 0x80000000u) ? ~u : (u | 0x80000000u);
; }
; __device__ void phase_q_route(KParams& p, int bid, int nb, char* smem) {
;     ...
; #pragma unroll
;         for (int i = 0; i < 2; ++i) {
;           uint32_t Kg[16];
; #pragma unroll
;           for (int g2 = 0; g2 < 16; ++g2)
;             Kg[g2] = (mono_key(Sa[i][g2]) & ~0x7Fu) | (uint32_t)((ih * 2 + i) * 32 + (g2 & 3) + 8 * (g2 >> 2)) | kb;
;           bitonic_sort16_desc(Kg);
	v_mfma_f32_32x32x16_bf16 v[2:17], v[214:217], v[38:41], v[2:17]
	v_min_u32_e32 v208, v200, v208
	v_cndmask_b32_e32 v19, v211, v210, vcc
	v_not_b32_e32 v210, v20
	v_or_b32_e32 v211, 0x80000000, v20
	v_cmp_gt_i32_e32 vcc, 0, v20
	v_max_u32_e32 v200, v218, v70
	v_min_u32_e32 v202, v218, v70
	v_cndmask_b32_e32 v20, v211, v210, vcc
	v_not_b32_e32 v210, v21
	v_or_b32_e32 v211, 0x80000000, v21
	v_cmp_gt_i32_e32 vcc, 0, v21
	s_nop 0
	v_not_b32_e32 v218, v2
	v_or_b32_e32 v219, 0x80000000, v2
	v_cndmask_b32_e32 v21, v211, v210, vcc
	v_not_b32_e32 v210, v22
	v_or_b32_e32 v211, 0x80000000, v22
	v_cmp_gt_i32_e32 vcc, 0, v22
	v_or_b32_e32 v220, 0x80000000, v5
	v_not_b32_e32 v221, v9
	v_cndmask_b32_e32 v22, v211, v210, vcc
	v_not_b32_e32 v210, v23
	v_or_b32_e32 v211, 0x80000000, v23
	v_cmp_gt_i32_e32 vcc, 0, v23
	v_or_b32_e32 v222, 0x80000000, v9
	v_or_b32_e32 v223, 0x80000000, v6
	v_cndmask_b32_e32 v23, v211, v210, vcc
	v_not_b32_e32 v210, v24
	v_or_b32_e32 v211, 0x80000000, v24
	v_cmp_gt_i32_e32 vcc, 0, v24
	v_not_b32_e32 v225, v17
	v_or_b32_e32 v226, 0x80000000, v17
	v_cndmask_b32_e32 v24, v211, v210, vcc
	v_not_b32_e32 v210, v25
	v_or_b32_e32 v211, 0x80000000, v25
	v_cmp_gt_i32_e32 vcc, 0, v25
	v_or_b32_e32 v227, 0x80000000, v14
	v_not_b32_e32 v228, v10
	v_cndmask_b32_e32 v25, v211, v210, vcc
	v_not_b32_e32 v210, v26
	v_or_b32_e32 v211, 0x80000000, v26
	v_cmp_gt_i32_e32 vcc, 0, v26
	v_or_b32_e32 v229, 0x80000000, v10
	v_or_b32_e32 v230, 0x80000000, v13
	v_cndmask_b32_e32 v26, v211, v210, vcc
	v_not_b32_e32 v210, v27
	v_or_b32_e32 v211, 0x80000000, v27
	v_cmp_gt_i32_e32 vcc, 0, v27
	v_and_or_b32 v18, v18, s3, v77
	v_and_or_b32 v19, v19, s3, v80
	v_cndmask_b32_e32 v27, v211, v210, vcc
	v_not_b32_e32 v210, v28
	v_or_b32_e32 v211, 0x80000000, v28
	v_cmp_gt_i32_e32 vcc, 0, v28
	v_and_or_b32 v20, v20, s3, v81
	v_and_or_b32 v21, v21, s3, v82
	v_cndmask_b32_e32 v28, v211, v210, vcc
	v_not_b32_e32 v210, v29
	v_or_b32_e32 v211, 0x80000000, v29
	v_cmp_gt_i32_e32 vcc, 0, v29
	v_and_or_b32 v22, v22, s3, v83
	v_and_or_b32 v23, v23, s3, v84
	v_cndmask_b32_e32 v29, v211, v210, vcc
	v_not_b32_e32 v210, v30
	v_or_b32_e32 v211, 0x80000000, v30
	v_cmp_gt_i32_e32 vcc, 0, v30
	v_and_or_b32 v24, v24, s3, v85
	v_and_or_b32 v25, v25, s3, v86
	v_cndmask_b32_e32 v30, v211, v210, vcc
	v_not_b32_e32 v210, v31
	v_or_b32_e32 v211, 0x80000000, v31
	v_cmp_gt_i32_e32 vcc, 0, v31
	v_and_or_b32 v26, v26, s3, v87
	v_and_or_b32 v27, v27, s3, v88
	v_cndmask_b32_e32 v31, v211, v210, vcc
	v_not_b32_e32 v210, v32
	v_or_b32_e32 v211, 0x80000000, v32
	v_cmp_gt_i32_e32 vcc, 0, v32
	v_and_or_b32 v28, v28, s3, v89
	v_and_or_b32 v29, v29, s3, v90
	v_cndmask_b32_e32 v32, v211, v210, vcc
	v_not_b32_e32 v210, v33
	v_or_b32_e32 v211, 0x80000000, v33
	v_cmp_gt_i32_e32 vcc, 0, v33
	v_and_or_b32 v30, v30, s3, v91
	v_and_or_b32 v31, v31, s3, v92
	v_cndmask_b32_e32 v33, v211, v210, vcc
	v_cmp_gt_i32_e32 vcc, 0, v2
	v_and_or_b32 v32, v32, s3, v93
	v_and_or_b32 v33, v33, s3, v94
	v_cndmask_b32_e32 v2, v219, v218, vcc
	v_not_b32_e32 v218, v3
	v_or_b32_e32 v219, 0x80000000, v3
	v_cmp_gt_i32_e32 vcc, 0, v3
	v_and_or_b32 v2, v2, s3, v95
	v_max_u32_e32 v210, v18, v19
	v_cndmask_b32_e32 v3, v219, v218, vcc
	v_not_b32_e32 v219, v5
	v_cmp_gt_i32_e32 vcc, 0, v5
	v_and_or_b32 v3, v3, s3, v96
	v_max_u32_e32 v218, v2, v3
	v_cndmask_b32_e32 v5, v220, v219, vcc
	v_not_b32_e32 v219, v4
	v_or_b32_e32 v220, 0x80000000, v4
	v_cmp_gt_i32_e32 vcc, 0, v4
	v_and_or_b32 v5, v5, s3, v97
	v_min_u32_e32 v2, v2, v3
	v_cndmask_b32_e32 v4, v220, v219, vcc
	v_cmp_gt_i32_e32 vcc, 0, v9
	v_and_or_b32 v4, v4, s3, v98
	v_min_u32_e32 v219, v5, v4
	v_cndmask_b32_e32 v9, v222, v221, vcc
	v_not_b32_e32 v221, v8
	v_or_b32_e32 v222, 0x80000000, v8
	v_cmp_gt_i32_e32 vcc, 0, v8
	v_and_or_b32 v9, v9, s3, v99
	v_max_u32_e32 v3, v5, v4
	v_cndmask_b32_e32 v8, v222, v221, vcc
	v_not_b32_e32 v222, v6
	v_cmp_gt_i32_e32 vcc, 0, v6
	v_and_or_b32 v8, v8, s3, v100
	v_max_u32_e32 v221, v9, v8
	v_cndmask_b32_e32 v6, v223, v222, vcc
	v_not_b32_e32 v222, v7
	v_or_b32_e32 v223, 0x80000000, v7
	v_cmp_gt_i32_e32 vcc, 0, v7
	v_and_or_b32 v6, v6, s3, v101
	v_min_u32_e32 v8, v9, v8
	v_cndmask_b32_e32 v7, v223, v222, vcc
	v_cmp_gt_i32_e32 vcc, 0, v17
	v_and_or_b32 v7, v7, s3, v102
	v_min_u32_e32 v222, v6, v7
	v_cndmask_b32_e32 v17, v226, v225, vcc
	v_not_b32_e32 v225, v16
	v_or_b32_e32 v226, 0x80000000, v16
	v_cmp_gt_i32_e32 vcc, 0, v16
	v_and_or_b32 v17, v17, s3, v103
	v_max_u32_e32 v6, v6, v7
	v_cndmask_b32_e32 v16, v226, v225, vcc
	v_not_b32_e32 v226, v14
	v_cmp_gt_i32_e32 vcc, 0, v14
	v_and_or_b32 v16, v16, s3, v104
	v_max_u32_e32 v225, v17, v16
	v_cndmask_b32_e32 v14, v227, v226, vcc
	v_not_b32_e32 v226, v15
	v_or_b32_e32 v227, 0x80000000, v15
	v_cmp_gt_i32_e32 vcc, 0, v15
	v_and_or_b32 v14, v14, s3, v105
	v_min_u32_e32 v16, v17, v16
	v_cndmask_b32_e32 v15, v227, v226, vcc
	v_cmp_gt_i32_e32 vcc, 0, v10
	v_and_or_b32 v15, v15, s3, v106
	v_min_u32_e32 v226, v14, v15
	v_cndmask_b32_e32 v10, v229, v228, vcc
	v_not_b32_e32 v228, v11
	v_or_b32_e32 v229, 0x80000000, v11
	v_cmp_gt_i32_e32 vcc, 0, v11
	v_and_or_b32 v10, v10, s3, v107
	v_max_u32_e32 v14, v14, v15
	v_cndmask_b32_e32 v11, v229, v228, vcc
	v_not_b32_e32 v229, v13
	v_cmp_gt_i32_e32 vcc, 0, v13
	v_and_or_b32 v11, v11, s3, v108
	v_max_u32_e32 v228, v10, v11
	v_cndmask_b32_e32 v13, v230, v229, vcc
	v_not_b32_e32 v229, v12
	v_or_b32_e32 v230, 0x80000000, v12
	v_cmp_gt_i32_e32 vcc, 0, v12
	v_and_or_b32 v13, v13, s3, v109
	v_min_u32_e32 v10, v10, v11
	v_cndmask_b32_e32 v12, v230, v229, vcc
	v_and_or_b32 v12, v12, s3, v110
	v_min_u32_e32 v229, v13, v12
	v_max_u32_e32 v11, v13, v12
	v_min_u32_e32 v18, v18, v19
; __device__ __forceinline__ void bitonic_sort16_desc(uint32_t (&K)[16]) {
; #pragma unroll
;   for (int k = 2; k <= 16; k <<= 1)
; #pragma unroll
;     for (int j = k >> 1; j >= 1; j >>= 1)
; #pragma unroll
;       for (int i = 0; i < 16; ++i) {
;         const int l = i ^ j;
;         if (l > i) { if ((i & k) == 0) ce_desc(K[i], K[l]); else ce_desc(K[l], K[i]); }
;       }
; }
	v_max_u32_e32 v19, v21, v20
	v_min_u32_e32 v20, v21, v20
	v_max_u32_e32 v21, v22, v23
	v_min_u32_e32 v22, v22, v23
	v_max_u32_e32 v23, v25, v24
	v_min_u32_e32 v24, v25, v24
	v_max_u32_e32 v25, v26, v27
	v_min_u32_e32 v26, v26, v27
	v_max_u32_e32 v27, v29, v28
	v_min_u32_e32 v28, v29, v28
	v_max_u32_e32 v29, v30, v31
	v_min_u32_e32 v30, v30, v31
	v_max_u32_e32 v31, v33, v32
	v_min_u32_e32 v32, v33, v32
	v_max_u32_e32 v220, v218, v219
	v_max_u32_e32 v4, v2, v3
	v_min_u32_e32 v223, v221, v222
	v_min_u32_e32 v7, v8, v6
	v_min_u32_e32 v218, v218, v219
	v_min_u32_e32 v2, v2, v3
	v_max_u32_e32 v219, v221, v222
	v_max_u32_e32 v6, v8, v6
	v_max_u32_e32 v227, v225, v226
	v_max_u32_e32 v15, v16, v14
	v_min_u32_e32 v230, v228, v229
	v_min_u32_e32 v12, v10, v11
	v_min_u32_e32 v225, v225, v226
	v_min_u32_e32 v14, v16, v14
	v_max_u32_e32 v226, v228, v229
	v_max_u32_e32 v10, v10, v11
	v_max_u32_e32 v33, v210, v20
	v_min_u32_e32 v20, v210, v20
	v_max_u32_e32 v210, v18, v19
	v_min_u32_e32 v18, v18, v19
	v_max_u32_e32 v19, v24, v21
	v_min_u32_e32 v21, v24, v21
	v_max_u32_e32 v24, v23, v22
	v_min_u32_e32 v22, v23, v22
	v_max_u32_e32 v23, v25, v28
	v_min_u32_e32 v25, v25, v28
	v_max_u32_e32 v28, v26, v27
	v_min_u32_e32 v26, v26, v27
	v_max_u32_e32 v27, v32, v29
	v_min_u32_e32 v29, v32, v29
	v_max_u32_e32 v32, v31, v30
	v_min_u32_e32 v30, v31, v30
	v_max_u32_e32 v5, v220, v4
	v_min_u32_e32 v9, v223, v7
	v_max_u32_e32 v3, v218, v2
	v_min_u32_e32 v8, v219, v6
	v_min_u32_e32 v4, v220, v4
	v_max_u32_e32 v7, v223, v7
	v_min_u32_e32 v2, v218, v2
	v_max_u32_e32 v6, v219, v6
	v_max_u32_e32 v17, v227, v15
	v_min_u32_e32 v13, v230, v12
	v_max_u32_e32 v16, v225, v14
	v_min_u32_e32 v11, v226, v10
	v_min_u32_e32 v15, v227, v15
	v_max_u32_e32 v12, v230, v12
	v_min_u32_e32 v14, v225, v14
	v_max_u32_e32 v10, v226, v10
	v_max_u32_e32 v31, v33, v210
	v_min_u32_e32 v33, v33, v210
	v_max_u32_e32 v210, v20, v18
	v_min_u32_e32 v18, v20, v18
	v_max_u32_e32 v20, v22, v21
	v_min_u32_e32 v21, v22, v21
	v_max_u32_e32 v22, v24, v19
	v_min_u32_e32 v19, v24, v19
	v_max_u32_e32 v24, v23, v28
	v_min_u32_e32 v23, v23, v28
	v_max_u32_e32 v28, v25, v26
	v_min_u32_e32 v25, v25, v26
	v_max_u32_e32 v26, v30, v29
	v_min_u32_e32 v29, v30, v29
	v_max_u32_e32 v30, v32, v27
	v_min_u32_e32 v27, v32, v27
	v_max_u32_e32 v224, v5, v9
	v_max_u32_e32 v221, v3, v8
	v_max_u32_e32 v220, v4, v7
	v_max_u32_e32 v218, v2, v6
	v_min_u32_e32 v231, v17, v13
	v_min_u32_e32 v228, v16, v11
	v_min_u32_e32 v227, v15, v12
	v_min_u32_e32 v225, v14, v10
	v_min_u32_e32 v5, v5, v9
	v_min_u32_e32 v3, v3, v8
	v_min_u32_e32 v4, v4, v7
	v_min_u32_e32 v2, v2, v6
	v_max_u32_e32 v9, v17, v13
	v_max_u32_e32 v11, v16, v11
	v_max_u32_e32 v12, v15, v12
	v_max_u32_e32 v10, v14, v10
	v_max_u32_e32 v32, v31, v21
	v_min_u32_e32 v21, v31, v21
	v_max_u32_e32 v31, v33, v20
	v_min_u32_e32 v20, v33, v20
	v_max_u32_e32 v33, v210, v19
	v_min_u32_e32 v19, v210, v19
	v_max_u32_e32 v210, v18, v22
	v_min_u32_e32 v18, v18, v22
	v_max_u32_e32 v22, v29, v24
	v_min_u32_e32 v24, v29, v24
	v_max_u32_e32 v29, v26, v23
	v_min_u32_e32 v23, v26, v23
	v_max_u32_e32 v26, v27, v28
	v_min_u32_e32 v27, v27, v28
	v_max_u32_e32 v28, v30, v25
	v_min_u32_e32 v25, v30, v25
	v_max_u32_e32 v222, v224, v221
	v_max_u32_e32 v219, v220, v218
	v_min_u32_e32 v229, v231, v228
	v_min_u32_e32 v226, v227, v225
	v_max_u32_e32 v8, v5, v3
	v_max_u32_e32 v6, v4, v2
	v_min_u32_e32 v13, v9, v11
	v_min_u32_e32 v14, v12, v10
	v_min_u32_e32 v221, v224, v221
	v_min_u32_e32 v218, v220, v218
	v_max_u32_e32 v224, v231, v228
	v_max_u32_e32 v225, v227, v225
	v_min_u32_e32 v3, v5, v3
	v_min_u32_e32 v2, v4, v2
	v_max_u32_e32 v5, v9, v11
	v_max_u32_e32 v9, v12, v10
	v_max_u32_e32 v30, v32, v33
	v_min_u32_e32 v32, v32, v33
	v_max_u32_e32 v33, v31, v210
	v_min_u32_e32 v31, v31, v210
	v_max_u32_e32 v210, v21, v19
	v_min_u32_e32 v19, v21, v19
	v_max_u32_e32 v21, v20, v18
	v_min_u32_e32 v18, v20, v18
	v_max_u32_e32 v20, v27, v24
	v_min_u32_e32 v24, v27, v24
	v_max_u32_e32 v27, v25, v23
	v_min_u32_e32 v23, v25, v23
	v_max_u32_e32 v25, v26, v22
	v_min_u32_e32 v22, v26, v22
	v_max_u32_e32 v26, v28, v29
	v_min_u32_e32 v28, v28, v29
	v_max_u32_e32 v223, v222, v219
	v_min_u32_e32 v230, v229, v226
	v_max_u32_e32 v7, v8, v6
	v_min_u32_e32 v15, v13, v14
	v_max_u32_e32 v220, v221, v218
	v_min_u32_e32 v227, v224, v225
	v_max_u32_e32 v4, v3, v2
	v_min_u32_e32 v10, v5, v9
	v_max_u32_e32 v29, v30, v33
	v_min_u32_e32 v30, v30, v33
	v_max_u32_e32 v33, v32, v31
	v_min_u32_e32 v31, v32, v31
	v_max_u32_e32 v32, v210, v21
	v_min_u32_e32 v21, v210, v21
	v_max_u32_e32 v210, v19, v18
	v_min_u32_e32 v18, v19, v18
	v_max_u32_e32 v19, v23, v24
	v_min_u32_e32 v23, v23, v24
	v_max_u32_e32 v24, v27, v20
	v_min_u32_e32 v20, v27, v20
	v_max_u32_e32 v27, v28, v22
	v_min_u32_e32 v22, v28, v22
	v_max_u32_e32 v28, v26, v25
	v_min_u32_e32 v25, v26, v25
	v_min_u32_e32 v232, v223, v230
	v_min_u32_e32 v16, v7, v15
	v_min_u32_e32 v228, v220, v227
	v_min_u32_e32 v11, v4, v10
	v_min_u32_e32 v219, v222, v219
	v_max_u32_e32 v222, v229, v226
	v_min_u32_e32 v6, v8, v6
	v_max_u32_e32 v8, v13, v14
	v_min_u32_e32 v218, v221, v218
	v_max_u32_e32 v221, v224, v225
	v_min_u32_e32 v2, v3, v2
	v_max_u32_e32 v3, v5, v9
	v_max_u32_e32 v26, v29, v23
	v_min_u32_e32 v23, v29, v23
	v_max_u32_e32 v29, v30, v19
	v_min_u32_e32 v19, v30, v19
	v_max_u32_e32 v30, v33, v20
	v_min_u32_e32 v20, v33, v20
	v_max_u32_e32 v33, v31, v24
	v_min_u32_e32 v24, v31, v24
	v_max_u32_e32 v31, v32, v22
	v_min_u32_e32 v22, v32, v22
	v_max_u32_e32 v32, v21, v27
	v_min_u32_e32 v21, v21, v27
	v_max_u32_e32 v27, v210, v25
	v_min_u32_e32 v25, v210, v25
	v_max_u32_e32 v210, v18, v28
; __device__ __forceinline__ void bitonic_sort16_desc(uint32_t (&K)[16]) {
; #pragma unroll
;   for (int k = 2; k <= 16; k <<= 1)
; #pragma unroll
;     for (int j = k >> 1; j >= 1; j >>= 1)
; #pragma unroll
;       for (int i = 0; i < 16; ++i) {
;         const int l = i ^ j;
;         if (l > i) { if ((i & k) == 0) ce_desc(K[i], K[l]); else ce_desc(K[l], K[i]); }
;       }
; }
; __device__ __forceinline__ void merge_top16(uint32_t (&Lk)[16], const uint32_t (&K)[16]) {
; #pragma unroll
;   for (int i = 0; i < 16; ++i) Lk[i] = max(Lk[i], K[15 - i]);
; #pragma unroll
;   for (int dd = 8; dd >= 1; dd >>= 1)
; #pragma unroll
;     for (int i = 0; i < 16; ++i)
;       if ((i & dd) == 0) ce_desc(Lk[i], Lk[i + dd]);
; }
; __device__ void phase_q_route(KParams& p, int bid, int nb, char* smem) {
;     ...
;         for (int ks = 0; ks < 4; ++ks) {
;           const bf16x8 qb = *reinterpret_cast<const bf16x8*>(smem + swz16(w * 32 + l31, sd * 8 + ks * 2 + lh));
; #pragma unroll
;           for (int i = 0; i < 2; ++i) {
;             const bf16x8 ka = *reinterpret_cast<const bf16x8*>(smem + 32768 + swz8(sd * 128 + (ih * 2 + i) * 32 + l31, ks * 2 + lh));
;             Sa[i] = __builtin_amdgcn_mfma_f32_32x32x16_bf16(ka, qb, Sa[i], 0, 0, 0);
;           }
	v_min_u32_e32 v18, v18, v28
	v_min_u32_e32 v17, v232, v16
	v_min_u32_e32 v12, v228, v11
	v_min_u32_e32 v226, v219, v222
	v_min_u32_e32 v13, v6, v8
	v_min_u32_e32 v224, v218, v221
	v_min_u32_e32 v5, v2, v3
	v_max_u32_e32 v16, v232, v16
	v_max_u32_e32 v11, v228, v11
	v_max_u32_e32 v28, v26, v31
	v_min_u32_e32 v26, v26, v31
	v_max_u32_e32 v31, v29, v32
	v_min_u32_e32 v29, v29, v32
	v_max_u32_e32 v32, v30, v27
	v_min_u32_e32 v27, v30, v27
	v_max_u32_e32 v30, v33, v210
	v_min_u32_e32 v33, v33, v210
	v_max_u32_e32 v210, v23, v22
	v_min_u32_e32 v22, v23, v22
	v_max_u32_e32 v23, v19, v21
	v_min_u32_e32 v19, v19, v21
	v_max_u32_e32 v21, v20, v25
	v_min_u32_e32 v20, v20, v25
	v_max_u32_e32 v25, v24, v18
	v_min_u32_e32 v231, v17, v12
	v_min_u32_e32 v14, v226, v13
	v_min_u32_e32 v9, v224, v5
	v_max_u32_e32 v12, v17, v12
	v_min_u32_e32 v17, v16, v11
	v_max_u32_e32 v11, v16, v11
	v_max_u32_e32 v16, v223, v230
	v_max_u32_e32 v7, v7, v15
	v_max_u32_e32 v220, v220, v227
	v_max_u32_e32 v4, v4, v10
	v_max_u32_e32 v219, v219, v222
	v_max_u32_e32 v6, v6, v8
	v_max_u32_e32 v218, v218, v221
	v_max_u32_e32 v2, v2, v3
	v_min_u32_e32 v18, v24, v18
	v_max_u32_e32 v24, v28, v32
	v_min_u32_e32 v28, v28, v32
	v_max_u32_e32 v32, v31, v30
	v_min_u32_e32 v30, v31, v30
	v_max_u32_e32 v31, v26, v27
	v_min_u32_e32 v26, v26, v27
	v_max_u32_e32 v27, v29, v33
	v_min_u32_e32 v29, v29, v33
	v_max_u32_e32 v33, v210, v21
	v_min_u32_e32 v21, v210, v21
	v_max_u32_e32 v210, v23, v25
	v_min_u32_e32 v225, v14, v9
	v_max_u32_e32 v13, v226, v13
	v_max_u32_e32 v5, v224, v5
	v_min_u32_e32 v15, v16, v7
	v_min_u32_e32 v10, v220, v4
	v_min_u32_e32 v8, v219, v6
	v_min_u32_e32 v3, v218, v2
	v_max_u32_e32 v7, v16, v7
	v_max_u32_e32 v4, v220, v4
	v_max_u32_e32 v6, v219, v6
	v_max_u32_e32 v2, v218, v2
	v_min_u32_e32 v23, v23, v25
	v_max_u32_e32 v25, v22, v20
	v_min_u32_e32 v20, v22, v20
	v_max_u32_e32 v22, v19, v18
	v_min_u32_e32 v18, v19, v18
	v_min_u32_e32 v19, v24, v32
	v_min_u32_e32 v214, v33, v210
	v_min_u32_e32 v229, v231, v225
	v_max_u32_e32 v9, v14, v9
	v_min_u32_e32 v224, v13, v5
	v_max_u32_e32 v5, v13, v5
	v_min_u32_e32 v223, v15, v10
	v_min_u32_e32 v221, v8, v3
	v_max_u32_e32 v10, v15, v10
	v_max_u32_e32 v3, v8, v3
	v_min_u32_e32 v15, v7, v4
	v_min_u32_e32 v16, v6, v2
	v_max_u32_e32 v4, v7, v4
	v_max_u32_e32 v2, v6, v2
	v_min_u32_e32 v211, v28, v30
	v_min_u32_e32 v212, v31, v27
	v_min_u32_e32 v213, v26, v29
	v_min_u32_e32 v215, v21, v23
	v_min_u32_e32 v14, v12, v9
	v_min_u32_e32 v226, v17, v224
	v_min_u32_e32 v13, v11, v5
	v_min_u32_e32 v222, v223, v221
	v_min_u32_e32 v8, v10, v3
	v_min_u32_e32 v218, v15, v16
	v_min_u32_e32 v6, v4, v2
	v_max3_u32 v7, v24, v32, v229
	v_max3_u32 v19, v19, v231, v225
	v_max3_u32 v24, v214, v223, v221
	v_min_u32_e32 v216, v25, v22
	v_min_u32_e32 v217, v20, v18
	v_max3_u32 v14, v28, v30, v14
	v_max3_u32 v9, v211, v12, v9
	v_max3_u32 v12, v31, v27, v226
	v_max3_u32 v17, v212, v17, v224
	v_max3_u32 v13, v26, v29, v13
	v_max3_u32 v5, v213, v11, v5
	v_max3_u32 v11, v33, v210, v222
	v_max3_u32 v8, v21, v23, v8
	v_max3_u32 v3, v215, v10, v3
	v_max3_u32 v10, v25, v22, v218
	v_max3_u32 v6, v20, v18, v6
	v_max_u32_e32 v212, v19, v24
	v_min_u32_e32 v213, v19, v24
	v_mfma_f32_32x32x16_bf16 v[18:33], v[62:65], v[58:61], 0
	ds_read_b128 v[62:65], v163 offset:57344
	v_max3_u32 v15, v216, v15, v16
	v_max3_u32 v2, v217, v4, v2
	v_max_u32_e32 v210, v7, v11
	v_min_u32_e32 v211, v7, v11
	v_max_u32_e32 v214, v14, v8
	v_min_u32_e32 v215, v14, v8
	v_max_u32_e32 v216, v9, v3
	v_min_u32_e32 v217, v9, v3
	v_max_u32_e32 v218, v12, v10
	v_min_u32_e32 v219, v12, v10
	v_max_u32_e32 v220, v17, v15
	v_min_u32_e32 v221, v17, v15
	v_max_u32_e32 v222, v13, v6
	v_min_u32_e32 v223, v13, v6
	v_max_u32_e32 v224, v5, v2
	v_min_u32_e32 v225, v5, v2
	v_mfma_f32_32x32x16_bf16 v[2:17], v[50:53], v[58:61], 0
	ds_read_b128 v[50:53], v163 offset:61440
	v_max_u32_e32 v226, v210, v218
	v_min_u32_e32 v58, v210, v218
	v_min_u32_e32 v210, v214, v222
	v_max_u32_e32 v59, v212, v220
	v_min_u32_e32 v60, v212, v220
	v_max_u32_e32 v212, v216, v224
	s_waitcnt lgkmcnt(1)
	v_mfma_f32_32x32x16_bf16 v[18:33], v[62:65], v[54:57], v[18:33]
	v_min_u32_e32 v62, v216, v224
	v_max_u32_e32 v63, v211, v219
	v_min_u32_e32 v64, v211, v219
	v_max_u32_e32 v65, v213, v221
	v_min_u32_e32 v211, v213, v221
	v_max_u32_e32 v61, v214, v222
	v_max_u32_e32 v213, v215, v223
	s_waitcnt lgkmcnt(0)
	v_mfma_f32_32x32x16_bf16 v[2:17], v[50:53], v[54:57], v[2:17]
	v_max_u32_e32 v56, v58, v210
	v_min_u32_e32 v57, v58, v210
	v_max_u32_e32 v50, v217, v225
	v_min_u32_e32 v51, v217, v225
	v_max_u32_e32 v54, v59, v212
	v_min_u32_e32 v55, v59, v212
	v_max_u32_e32 v58, v60, v62
	v_mfma_f32_32x32x16_bf16 v[18:33], v[34:37], v[42:45], v[18:33]
	ds_read_b128 v[34:37], v167 offset:57344
	v_min_u32_e32 v59, v60, v62
	v_max_u32_e32 v62, v65, v50
	v_max_u32_e32 v52, v226, v61
	v_min_u32_e32 v53, v226, v61
	v_max_u32_e32 v60, v63, v213
	v_min_u32_e32 v61, v63, v213
	v_mfma_f32_32x32x16_bf16 v[2:17], v[46:49], v[42:45], v[2:17]
	ds_read_b128 v[42:45], v167 offset:61440
	v_min_u32_e32 v46, v65, v50
	v_max_u32_e32 v49, v211, v51
	v_min_u32_e32 v50, v211, v51
	v_min_u32_e32 v214, v215, v223
	v_max_u32_e32 v47, v64, v214
	v_min_u32_e32 v48, v64, v214
	s_waitcnt lgkmcnt(1)
	v_mfma_f32_32x32x16_bf16 v[18:33], v[34:37], v[38:41], v[18:33]
	v_min_u32_e32 v34, v53, v55
	v_min_u32_e32 v36, v57, v59
	v_min_u32_e32 v37, v60, v62
	v_min_u32_e32 v35, v56, v58
	v_min_u32_e32 v51, v52, v54
	v_min_u32_e32 v63, v61, v46
	v_min_u32_e32 v64, v47, v49
	s_waitcnt lgkmcnt(0)
; __device__ __forceinline__ uint32_t mono_key(float f) {
;   uint32_t u = __float_as_uint(f);
;   return (u & 0x80000000u) ? ~u : (u | 0x80000000u);
; }
; __device__ __forceinline__ void bitonic_sort16_desc(uint32_t (&K)[16]) {
; #pragma unroll
;   for (int k = 2; k <= 16; k <<= 1)
; #pragma unroll
;     for (int j = k >> 1; j >= 1; j >>= 1)
; #pragma unroll
;       for (int i = 0; i < 16; ++i) {
;         const int l = i ^ j;
;         if (l > i) { if ((i & k) == 0) ce_desc(K[i], K[l]); else ce_desc(K[l], K[i]); }
;       }
; }
; __device__ void phase_q_route(KParams& p, int bid, int nb, char* smem) {
;     ...
; #pragma unroll
;         for (int i = 0; i < 2; ++i) {
;           uint32_t Kg[16];
; #pragma unroll
;           for (int g2 = 0; g2 < 16; ++g2)
;             Kg[g2] = (mono_key(Sa[i][g2]) & ~0x7Fu) | (uint32_t)((ih * 2 + i) * 32 + (g2 & 3) + 8 * (g2 >> 2)) | kb;
;           bitonic_sort16_desc(Kg);
	v_mfma_f32_32x32x16_bf16 v[2:17], v[42:45], v[38:41], v[2:17]
	s_nop 2
	v_not_b32_e32 v38, v18
	v_or_b32_e32 v39, 0x80000000, v18
	v_cmp_gt_i32_e32 vcc, 0, v18
	v_or_b32_e32 v40, 0x80000000, v21
	v_not_b32_e32 v41, v25
	v_cndmask_b32_e32 v18, v39, v38, vcc
	v_not_b32_e32 v38, v19
	v_or_b32_e32 v39, 0x80000000, v19
	v_cmp_gt_i32_e32 vcc, 0, v19
	v_or_b32_e32 v42, 0x80000000, v25
	v_or_b32_e32 v43, 0x80000000, v22
	v_cndmask_b32_e32 v19, v39, v38, vcc
	v_not_b32_e32 v39, v21
	v_cmp_gt_i32_e32 vcc, 0, v21
	v_not_b32_e32 v45, v33
	v_or_b32_e32 v210, 0x80000000, v33
	v_cndmask_b32_e32 v21, v40, v39, vcc
	v_not_b32_e32 v39, v20
	v_or_b32_e32 v40, 0x80000000, v20
	v_cmp_gt_i32_e32 vcc, 0, v20
	v_or_b32_e32 v211, 0x80000000, v30
	v_not_b32_e32 v212, v26
	v_cndmask_b32_e32 v20, v40, v39, vcc
	v_cmp_gt_i32_e32 vcc, 0, v25
	v_or_b32_e32 v213, 0x80000000, v26
	v_or_b32_e32 v214, 0x80000000, v29
	v_cndmask_b32_e32 v25, v42, v41, vcc
	v_not_b32_e32 v41, v24
	v_or_b32_e32 v42, 0x80000000, v24
	v_cmp_gt_i32_e32 vcc, 0, v24
	v_and_or_b32 v18, v18, s3, v111
	v_and_or_b32 v19, v19, s3, v112
	v_cndmask_b32_e32 v24, v42, v41, vcc
	v_not_b32_e32 v42, v22
	v_cmp_gt_i32_e32 vcc, 0, v22
	v_and_or_b32 v21, v21, s3, v113
	v_and_or_b32 v20, v20, s3, v114
	v_cndmask_b32_e32 v22, v43, v42, vcc
	v_not_b32_e32 v42, v23
	v_or_b32_e32 v43, 0x80000000, v23
	v_cmp_gt_i32_e32 vcc, 0, v23
	v_and_or_b32 v25, v25, s3, v115
	v_and_or_b32 v24, v24, s3, v116
	v_cndmask_b32_e32 v23, v43, v42, vcc
	v_cmp_gt_i32_e32 vcc, 0, v33
	v_and_or_b32 v22, v22, s3, v117
	v_and_or_b32 v23, v23, s3, v118
	v_cndmask_b32_e32 v33, v210, v45, vcc
	v_not_b32_e32 v45, v32
	v_or_b32_e32 v210, 0x80000000, v32
	v_cmp_gt_i32_e32 vcc, 0, v32
	v_and_or_b32 v33, v33, s3, v119
	v_max_u32_e32 v38, v18, v19
	v_cndmask_b32_e32 v32, v210, v45, vcc
	v_not_b32_e32 v210, v30
	v_cmp_gt_i32_e32 vcc, 0, v30
	v_and_or_b32 v32, v32, s3, v120
	v_min_u32_e32 v39, v21, v20
	v_cndmask_b32_e32 v30, v211, v210, vcc
	v_not_b32_e32 v210, v31
	v_or_b32_e32 v211, 0x80000000, v31
	v_cmp_gt_i32_e32 vcc, 0, v31
	v_and_or_b32 v30, v30, s3, v121
	v_min_u32_e32 v18, v18, v19
	v_cndmask_b32_e32 v31, v211, v210, vcc
	v_cmp_gt_i32_e32 vcc, 0, v26
	v_and_or_b32 v31, v31, s3, v122
	v_max_u32_e32 v19, v21, v20
	v_cndmask_b32_e32 v26, v213, v212, vcc
	v_not_b32_e32 v212, v27
	v_or_b32_e32 v213, 0x80000000, v27
	v_cmp_gt_i32_e32 vcc, 0, v27
	v_and_or_b32 v26, v26, s3, v123
	v_max_u32_e32 v41, v25, v24
	v_cndmask_b32_e32 v27, v213, v212, vcc
	v_not_b32_e32 v213, v29
	v_cmp_gt_i32_e32 vcc, 0, v29
	v_and_or_b32 v27, v27, s3, v124
	v_min_u32_e32 v42, v22, v23
	v_cndmask_b32_e32 v29, v214, v213, vcc
	v_not_b32_e32 v213, v28
	v_or_b32_e32 v214, 0x80000000, v28
	v_cmp_gt_i32_e32 vcc, 0, v28
	v_and_or_b32 v29, v29, s3, v125
	v_min_u32_e32 v24, v25, v24
	v_cndmask_b32_e32 v28, v214, v213, vcc
	v_and_or_b32 v28, v28, s3, v126
	v_max_u32_e32 v22, v22, v23
	v_max_u32_e32 v45, v33, v32
	v_min_u32_e32 v210, v30, v31
	v_min_u32_e32 v32, v33, v32
	v_max_u32_e32 v30, v30, v31
	v_max_u32_e32 v212, v26, v27
	v_min_u32_e32 v213, v29, v28
	v_min_u32_e32 v26, v26, v27
	v_max_u32_e32 v27, v29, v28
	v_max_u32_e32 v40, v38, v39
	v_max_u32_e32 v20, v18, v19
	v_min_u32_e32 v43, v41, v42
	v_min_u32_e32 v23, v24, v22
	v_min_u32_e32 v38, v38, v39
	v_min_u32_e32 v18, v18, v19
	v_max_u32_e32 v39, v41, v42
	v_max_u32_e32 v22, v24, v22
	v_max_u32_e32 v211, v45, v210
	v_max_u32_e32 v31, v32, v30
	v_min_u32_e32 v214, v212, v213
	v_min_u32_e32 v28, v26, v27
	v_min_u32_e32 v45, v45, v210
	v_min_u32_e32 v30, v32, v30
	v_max_u32_e32 v210, v212, v213
	v_max_u32_e32 v26, v26, v27
	v_max_u32_e32 v21, v40, v20
	v_min_u32_e32 v25, v43, v23
	v_max_u32_e32 v19, v38, v18
	v_min_u32_e32 v24, v39, v22
	v_min_u32_e32 v20, v40, v20
	v_max_u32_e32 v23, v43, v23
	v_min_u32_e32 v18, v38, v18
	v_max_u32_e32 v22, v39, v22
	v_max_u32_e32 v33, v211, v31
	v_min_u32_e32 v29, v214, v28
	v_max_u32_e32 v32, v45, v30
	v_min_u32_e32 v27, v210, v26
	v_min_u32_e32 v31, v211, v31
	v_max_u32_e32 v28, v214, v28
	v_min_u32_e32 v30, v45, v30
	v_max_u32_e32 v26, v210, v26
	v_max_u32_e32 v44, v21, v25
	v_max_u32_e32 v41, v19, v24
	v_max_u32_e32 v40, v20, v23
	v_max_u32_e32 v38, v18, v22
	v_min_u32_e32 v215, v33, v29
	v_min_u32_e32 v212, v32, v27
	v_min_u32_e32 v211, v31, v28
	v_min_u32_e32 v45, v30, v26
	v_min_u32_e32 v21, v21, v25
	v_min_u32_e32 v19, v19, v24
	v_min_u32_e32 v20, v20, v23
	v_min_u32_e32 v18, v18, v22
	v_max_u32_e32 v25, v33, v29
	v_max_u32_e32 v27, v32, v27
	v_max_u32_e32 v28, v31, v28
	v_max_u32_e32 v26, v30, v26
	v_max_u32_e32 v42, v44, v41
	v_max_u32_e32 v39, v40, v38
	v_min_u32_e32 v213, v215, v212
	v_min_u32_e32 v210, v211, v45
	v_max_u32_e32 v24, v21, v19
	v_max_u32_e32 v22, v20, v18
	v_min_u32_e32 v29, v25, v27
	v_min_u32_e32 v30, v28, v26
	v_min_u32_e32 v41, v44, v41
	v_min_u32_e32 v38, v40, v38
	v_max_u32_e32 v44, v215, v212
	v_max_u32_e32 v45, v211, v45
	v_min_u32_e32 v19, v21, v19
	v_min_u32_e32 v18, v20, v18
	v_max_u32_e32 v21, v25, v27
	v_max_u32_e32 v25, v28, v26
	v_max_u32_e32 v43, v42, v39
	v_min_u32_e32 v214, v213, v210
	v_max_u32_e32 v23, v24, v22
	v_min_u32_e32 v31, v29, v30
	v_max_u32_e32 v40, v41, v38
	v_min_u32_e32 v211, v44, v45
	v_max_u32_e32 v20, v19, v18
	v_min_u32_e32 v26, v21, v25
	v_min_u32_e32 v216, v43, v214
	v_min_u32_e32 v32, v23, v31
	v_min_u32_e32 v212, v40, v211
	v_min_u32_e32 v27, v20, v26
	v_min_u32_e32 v33, v216, v32
	v_min_u32_e32 v28, v212, v27
	v_min_u32_e32 v39, v42, v39
	v_max_u32_e32 v42, v213, v210
	v_min_u32_e32 v22, v24, v22
	v_max_u32_e32 v24, v29, v30
	v_min_u32_e32 v38, v41, v38
	v_max_u32_e32 v41, v44, v45
	v_min_u32_e32 v18, v19, v18
; __device__ __forceinline__ void bitonic_sort16_desc(uint32_t (&K)[16]) {
; #pragma unroll
;   for (int k = 2; k <= 16; k <<= 1)
; #pragma unroll
;     for (int j = k >> 1; j >= 1; j >>= 1)
; #pragma unroll
;       for (int i = 0; i < 16; ++i) {
;         const int l = i ^ j;
;         if (l > i) { if ((i & k) == 0) ce_desc(K[i], K[l]); else ce_desc(K[l], K[i]); }
;       }
; }
; __device__ __forceinline__ void merge_top16(uint32_t (&Lk)[16], const uint32_t (&K)[16]) {
; #pragma unroll
;   for (int i = 0; i < 16; ++i) Lk[i] = max(Lk[i], K[15 - i]);
; #pragma unroll
;   for (int dd = 8; dd >= 1; dd >>= 1)
; #pragma unroll
;     for (int i = 0; i < 16; ++i)
;       if ((i & dd) == 0) ce_desc(Lk[i], Lk[i + dd]);
; }
; __device__ void phase_q_route(KParams& p, int bid, int nb, char* smem) {
;     ...
;             Kg[g2] = (mono_key(Sa[i][g2]) & ~0x7Fu) | (uint32_t)((ih * 2 + i) * 32 + (g2 & 3) + 8 * (g2 >> 2)) | kb;
	v_max_u32_e32 v19, v21, v25
	v_max_u32_e32 v32, v216, v32
	v_max_u32_e32 v27, v212, v27
	v_min_u32_e32 v215, v33, v28
	v_min_u32_e32 v210, v39, v42
	v_min_u32_e32 v29, v22, v24
	v_min_u32_e32 v44, v38, v41
	v_min_u32_e32 v21, v18, v19
	v_max_u32_e32 v28, v33, v28
	v_min_u32_e32 v33, v32, v27
	v_max_u32_e32 v27, v32, v27
	v_max_u32_e32 v32, v43, v214
	v_max_u32_e32 v23, v23, v31
	v_max_u32_e32 v40, v40, v211
	v_max_u32_e32 v20, v20, v26
	v_max_u32_e32 v39, v39, v42
	v_max_u32_e32 v22, v22, v24
	v_max_u32_e32 v38, v38, v41
	v_max_u32_e32 v18, v18, v19
	v_min_u32_e32 v31, v32, v23
	v_min_u32_e32 v26, v40, v20
	v_min_u32_e32 v24, v39, v22
	v_min_u32_e32 v19, v38, v18
	v_min_u32_e32 v30, v210, v29
	v_min_u32_e32 v25, v44, v21
	v_max_u32_e32 v29, v210, v29
	v_max_u32_e32 v21, v44, v21
	v_min_u32_e32 v43, v31, v26
	v_min_u32_e32 v41, v24, v19
	v_min_u32_e32 v45, v30, v25
	v_max_u32_e32 v25, v30, v25
	v_min_u32_e32 v44, v29, v21
	v_max_u32_e32 v21, v29, v21
	v_min_u32_e32 v42, v43, v41
	v_min_u32_e32 v30, v28, v25
	v_min_u32_e32 v29, v27, v21
	v_max3_u32 v25, v34, v28, v25
	v_max3_u32 v21, v36, v27, v21
	v_max3_u32 v27, v60, v62, v42
	v_max3_u32 v34, v37, v43, v41
	v_not_b32_e32 v42, v2
	v_or_b32_e32 v43, 0x80000000, v2
	v_cmp_gt_i32_e32 vcc, 0, v2
	v_min_u32_e32 v210, v33, v44
	v_max_u32_e32 v26, v31, v26
	v_cndmask_b32_e32 v2, v43, v42, vcc
	v_not_b32_e32 v42, v3
	v_or_b32_e32 v43, 0x80000000, v3
	v_cmp_gt_i32_e32 vcc, 0, v3
	v_max_u32_e32 v19, v24, v19
	v_max3_u32 v33, v35, v33, v44
	v_cndmask_b32_e32 v3, v43, v42, vcc
	v_not_b32_e32 v43, v5
	v_or_b32_e32 v44, 0x80000000, v5
	v_cmp_gt_i32_e32 vcc, 0, v5
	v_min_u32_e32 v24, v26, v19
	v_max_u32_e32 v23, v32, v23
	v_max_u32_e32 v20, v40, v20
	v_max_u32_e32 v22, v39, v22
	v_max_u32_e32 v18, v38, v18
	v_cndmask_b32_e32 v5, v44, v43, vcc
	v_not_b32_e32 v43, v4
	v_or_b32_e32 v44, 0x80000000, v4
	v_cmp_gt_i32_e32 vcc, 0, v4
	v_min_u32_e32 v213, v215, v45
	v_min_u32_e32 v31, v23, v20
	v_min_u32_e32 v32, v22, v18
	v_max3_u32 v39, v51, v215, v45
	v_max3_u32 v24, v61, v46, v24
	v_cndmask_b32_e32 v4, v44, v43, vcc
	v_not_b32_e32 v45, v9
	v_or_b32_e32 v46, 0x80000000, v9
	v_cmp_gt_i32_e32 vcc, 0, v9
	v_min_u32_e32 v38, v31, v32
	v_max_u32_e32 v20, v23, v20
	v_cndmask_b32_e32 v9, v46, v45, vcc
	v_not_b32_e32 v45, v8
	v_or_b32_e32 v46, 0x80000000, v8
	v_cmp_gt_i32_e32 vcc, 0, v8
	v_max_u32_e32 v18, v22, v18
	v_max3_u32 v19, v63, v26, v19
	v_max3_u32 v26, v47, v49, v38
	v_cndmask_b32_e32 v8, v46, v45, vcc
	v_not_b32_e32 v46, v6
	v_or_b32_e32 v47, 0x80000000, v6
	v_cmp_gt_i32_e32 vcc, 0, v6
	v_min_u32_e32 v22, v20, v18
	v_min_u32_e32 v65, v48, v50
	v_cndmask_b32_e32 v6, v47, v46, vcc
	v_not_b32_e32 v46, v7
	v_or_b32_e32 v47, 0x80000000, v7
	v_cmp_gt_i32_e32 vcc, 0, v7
	v_max3_u32 v22, v48, v50, v22
	v_not_b32_e32 v49, v17
	v_cndmask_b32_e32 v7, v47, v46, vcc
	v_or_b32_e32 v50, 0x80000000, v17
	v_cmp_gt_i32_e32 vcc, 0, v17
	v_or_b32_e32 v51, 0x80000000, v14
	v_max3_u32 v23, v52, v54, v213
	v_cndmask_b32_e32 v17, v50, v49, vcc
	v_not_b32_e32 v49, v16
	v_or_b32_e32 v50, 0x80000000, v16
	v_cmp_gt_i32_e32 vcc, 0, v16
	v_max3_u32 v30, v53, v55, v30
	v_not_b32_e32 v52, v10
	v_cndmask_b32_e32 v16, v50, v49, vcc
	v_not_b32_e32 v50, v14
	v_cmp_gt_i32_e32 vcc, 0, v14
	v_or_b32_e32 v53, 0x80000000, v10
	v_or_b32_e32 v54, 0x80000000, v13
	v_cndmask_b32_e32 v14, v51, v50, vcc
	v_not_b32_e32 v50, v15
	v_or_b32_e32 v51, 0x80000000, v15
	v_cmp_gt_i32_e32 vcc, 0, v15
	v_and_or_b32 v2, v2, s3, v127
	v_and_or_b32 v3, v3, s3, v128
	v_cndmask_b32_e32 v15, v51, v50, vcc
	v_cmp_gt_i32_e32 vcc, 0, v10
	v_and_or_b32 v5, v5, s3, v129
	v_and_or_b32 v4, v4, s3, v130
	v_cndmask_b32_e32 v10, v53, v52, vcc
	v_not_b32_e32 v52, v11
	v_or_b32_e32 v53, 0x80000000, v11
	v_cmp_gt_i32_e32 vcc, 0, v11
	v_and_or_b32 v9, v9, s3, v131
	v_and_or_b32 v8, v8, s3, v132
	v_cndmask_b32_e32 v11, v53, v52, vcc
	v_not_b32_e32 v53, v13
	v_cmp_gt_i32_e32 vcc, 0, v13
	v_and_or_b32 v6, v6, s3, v133
	v_and_or_b32 v7, v7, s3, v134
	v_cndmask_b32_e32 v13, v54, v53, vcc
	v_not_b32_e32 v53, v12
	v_or_b32_e32 v54, 0x80000000, v12
	v_cmp_gt_i32_e32 vcc, 0, v12
	v_and_or_b32 v17, v17, s3, v135
	v_and_or_b32 v16, v16, s3, v136
	v_cndmask_b32_e32 v12, v54, v53, vcc
	v_and_or_b32 v14, v14, s3, v137
	v_and_or_b32 v15, v15, s3, v138
	v_and_or_b32 v10, v10, s3, v139
	v_and_or_b32 v11, v11, s3, v140
	v_and_or_b32 v13, v13, s3, v141
	v_and_or_b32 v12, v12, s3, v142
	v_max_u32_e32 v42, v2, v3
	v_min_u32_e32 v43, v5, v4
	v_min_u32_e32 v2, v2, v3
	v_max_u32_e32 v3, v5, v4
	v_max_u32_e32 v45, v9, v8
	v_min_u32_e32 v46, v6, v7
	v_min_u32_e32 v8, v9, v8
	v_max_u32_e32 v6, v6, v7
	v_max_u32_e32 v49, v17, v16
	v_min_u32_e32 v50, v14, v15
	v_min_u32_e32 v16, v17, v16
	v_max_u32_e32 v14, v14, v15
	v_max_u32_e32 v52, v10, v11
	v_min_u32_e32 v53, v13, v12
	v_min_u32_e32 v10, v10, v11
	v_max_u32_e32 v11, v13, v12
	v_max_u32_e32 v44, v42, v43
	v_max_u32_e32 v4, v2, v3
	v_min_u32_e32 v47, v45, v46
	v_min_u32_e32 v7, v8, v6
	v_min_u32_e32 v42, v42, v43
	v_min_u32_e32 v2, v2, v3
	v_max_u32_e32 v43, v45, v46
	v_max_u32_e32 v6, v8, v6
	v_max_u32_e32 v51, v49, v50
	v_max_u32_e32 v15, v16, v14
	v_min_u32_e32 v54, v52, v53
	v_min_u32_e32 v12, v10, v11
	v_min_u32_e32 v49, v49, v50
	v_min_u32_e32 v14, v16, v14
	v_max_u32_e32 v50, v52, v53
	v_max_u32_e32 v10, v10, v11
	v_max_u32_e32 v5, v44, v4
	v_min_u32_e32 v9, v47, v7
	v_max_u32_e32 v3, v42, v2
	v_min_u32_e32 v8, v43, v6
	v_min_u32_e32 v4, v44, v4
	v_max_u32_e32 v7, v47, v7
	v_min_u32_e32 v2, v42, v2
	v_max_u32_e32 v6, v43, v6
	v_max_u32_e32 v17, v51, v15
	v_min_u32_e32 v13, v54, v12
	v_max_u32_e32 v16, v49, v14
	v_min_u32_e32 v11, v50, v10
; __device__ __forceinline__ void bitonic_sort16_desc(uint32_t (&K)[16]) {
; #pragma unroll
;   for (int k = 2; k <= 16; k <<= 1)
; #pragma unroll
;     for (int j = k >> 1; j >= 1; j >>= 1)
; #pragma unroll
;       for (int i = 0; i < 16; ++i) {
;         const int l = i ^ j;
;         if (l > i) { if ((i & k) == 0) ce_desc(K[i], K[l]); else ce_desc(K[l], K[i]); }
;       }
; }
; __device__ __forceinline__ void merge_top16(uint32_t (&Lk)[16], const uint32_t (&K)[16]) {
; #pragma unroll
;   for (int i = 0; i < 16; ++i) Lk[i] = max(Lk[i], K[15 - i]);
; #pragma unroll
;   for (int dd = 8; dd >= 1; dd >>= 1)
; #pragma unroll
;     for (int i = 0; i < 16; ++i)
;       if ((i & dd) == 0) ce_desc(Lk[i], Lk[i + dd]);
; }
	v_min_u32_e32 v15, v51, v15
	v_max_u32_e32 v12, v54, v12
	v_min_u32_e32 v14, v49, v14
	v_max_u32_e32 v10, v50, v10
	v_max_u32_e32 v48, v5, v9
	v_max_u32_e32 v45, v3, v8
	v_max_u32_e32 v44, v4, v7
	v_max_u32_e32 v42, v2, v6
	v_min_u32_e32 v55, v17, v13
	v_min_u32_e32 v52, v16, v11
	v_min_u32_e32 v51, v15, v12
	v_min_u32_e32 v49, v14, v10
	v_min_u32_e32 v5, v5, v9
	v_min_u32_e32 v3, v3, v8
	v_min_u32_e32 v4, v4, v7
	v_min_u32_e32 v2, v2, v6
	v_max_u32_e32 v9, v17, v13
	v_max_u32_e32 v11, v16, v11
	v_max_u32_e32 v12, v15, v12
	v_max_u32_e32 v10, v14, v10
	v_max_u32_e32 v46, v48, v45
	v_max_u32_e32 v43, v44, v42
	v_min_u32_e32 v53, v55, v52
	v_min_u32_e32 v50, v51, v49
	v_max_u32_e32 v8, v5, v3
	v_max_u32_e32 v6, v4, v2
	v_min_u32_e32 v13, v9, v11
	v_min_u32_e32 v14, v12, v10
	v_min_u32_e32 v45, v48, v45
	v_min_u32_e32 v42, v44, v42
	v_max_u32_e32 v48, v55, v52
	v_max_u32_e32 v49, v51, v49
	v_min_u32_e32 v3, v5, v3
	v_min_u32_e32 v2, v4, v2
	v_max_u32_e32 v5, v9, v11
	v_max_u32_e32 v9, v12, v10
	v_max_u32_e32 v47, v46, v43
	v_min_u32_e32 v54, v53, v50
	v_max_u32_e32 v7, v8, v6
	v_min_u32_e32 v15, v13, v14
	v_max_u32_e32 v44, v45, v42
	v_min_u32_e32 v51, v48, v49
	v_max_u32_e32 v4, v3, v2
	v_min_u32_e32 v10, v5, v9
	v_min_u32_e32 v43, v46, v43
	v_max_u32_e32 v46, v53, v50
	v_min_u32_e32 v6, v8, v6
	v_max_u32_e32 v8, v13, v14
	v_min_u32_e32 v42, v45, v42
	v_max_u32_e32 v45, v48, v49
	v_min_u32_e32 v2, v3, v2
	v_max_u32_e32 v3, v5, v9
	v_max3_u32 v28, v56, v58, v210
	v_max3_u32 v29, v57, v59, v29
	v_max3_u32 v31, v64, v31, v32
	v_max3_u32 v18, v65, v20, v18
	v_min_u32_e32 v56, v47, v54
	v_min_u32_e32 v16, v7, v15
	v_min_u32_e32 v52, v44, v51
	v_min_u32_e32 v11, v4, v10
	v_min_u32_e32 v50, v43, v46
	v_min_u32_e32 v13, v6, v8
	v_min_u32_e32 v48, v42, v45
	v_min_u32_e32 v5, v2, v3
	v_max_u32_e32 v20, v23, v27
	v_min_u32_e32 v23, v23, v27
	v_max_u32_e32 v27, v39, v34
	v_min_u32_e32 v32, v39, v34
	v_max_u32_e32 v34, v30, v24
	v_min_u32_e32 v24, v30, v24
	v_max_u32_e32 v30, v25, v19
	v_min_u32_e32 v19, v25, v19
	v_max_u32_e32 v25, v28, v26
	v_min_u32_e32 v26, v28, v26
	v_max_u32_e32 v28, v33, v31
	v_min_u32_e32 v31, v33, v31
	v_max_u32_e32 v33, v29, v22
	v_min_u32_e32 v22, v29, v22
	v_max_u32_e32 v29, v21, v18
	v_min_u32_e32 v17, v56, v16
	v_min_u32_e32 v12, v52, v11
	v_min_u32_e32 v14, v50, v13
	v_min_u32_e32 v9, v48, v5
	v_min_u32_e32 v18, v21, v18
	v_max_u32_e32 v21, v20, v25
	v_min_u32_e32 v20, v20, v25
	v_max_u32_e32 v25, v27, v28
	v_min_u32_e32 v27, v27, v28
	v_max_u32_e32 v28, v34, v33
	v_min_u32_e32 v33, v34, v33
	v_max_u32_e32 v34, v30, v29
	v_min_u32_e32 v55, v17, v12
	v_min_u32_e32 v49, v14, v9
	v_min_u32_e32 v29, v30, v29
	v_max_u32_e32 v30, v23, v26
	v_min_u32_e32 v23, v23, v26
	v_max_u32_e32 v26, v32, v31
	v_min_u32_e32 v31, v32, v31
	v_max_u32_e32 v32, v24, v22
	v_min_u32_e32 v22, v24, v22
	v_max_u32_e32 v24, v19, v18
	v_min_u32_e32 v18, v19, v18
	v_max_u32_e32 v19, v21, v28
	v_min_u32_e32 v21, v21, v28
	v_max_u32_e32 v28, v25, v34
	v_min_u32_e32 v53, v55, v49
	v_min_u32_e32 v25, v25, v34
	v_max_u32_e32 v34, v20, v33
	v_min_u32_e32 v20, v20, v33
	v_max_u32_e32 v33, v27, v29
	v_min_u32_e32 v27, v27, v29
	v_max_u32_e32 v29, v30, v32
	v_min_u32_e32 v30, v30, v32
	v_max_u32_e32 v32, v26, v24
	v_min_u32_e32 v24, v26, v24
	v_max_u32_e32 v26, v23, v22
	v_min_u32_e32 v22, v23, v22
	v_max_u32_e32 v23, v31, v18
	v_min_u32_e32 v18, v31, v18
	v_min_u32_e32 v31, v19, v28
	v_max3_u32 v19, v19, v28, v53
	v_max_u32_e32 v28, v47, v54
	v_max_u32_e32 v7, v7, v15
	v_max_u32_e32 v44, v44, v51
	v_max_u32_e32 v4, v4, v10
	v_max_u32_e32 v43, v43, v46
	v_max_u32_e32 v6, v6, v8
	v_max_u32_e32 v42, v42, v45
	v_max_u32_e32 v2, v2, v3
	v_min_u32_e32 v15, v28, v7
	v_min_u32_e32 v10, v44, v4
	v_min_u32_e32 v8, v43, v6
	v_min_u32_e32 v3, v42, v2
	v_min_u32_e32 v47, v15, v10
	v_min_u32_e32 v45, v8, v3
	v_min_u32_e32 v46, v47, v45
	v_max_u32_e32 v16, v56, v16
	v_max_u32_e32 v11, v52, v11
	v_max_u32_e32 v13, v50, v13
	v_max_u32_e32 v5, v48, v5
	v_min_u32_e32 v38, v29, v32
	v_max3_u32 v29, v29, v32, v46
	v_min_u32_e32 v46, v16, v11
	v_min_u32_e32 v48, v13, v5
	v_min_u32_e32 v50, v46, v48
	v_max_u32_e32 v7, v28, v7
	v_max_u32_e32 v4, v44, v4
	v_max_u32_e32 v6, v43, v6
	v_max_u32_e32 v2, v42, v2
	v_min_u32_e32 v36, v34, v33
	v_max3_u32 v33, v34, v33, v50
	v_min_u32_e32 v28, v7, v4
	v_min_u32_e32 v34, v6, v2
	v_max_u32_e32 v12, v17, v12
	v_max_u32_e32 v9, v14, v9
	v_max_u32_e32 v10, v15, v10
	v_max_u32_e32 v3, v8, v3
	v_max_u32_e32 v11, v16, v11
	v_max_u32_e32 v5, v13, v5
	v_max_u32_e32 v4, v7, v4
	v_max_u32_e32 v2, v6, v2
	v_min_u32_e32 v35, v21, v25
	v_min_u32_e32 v37, v20, v27
	v_min_u32_e32 v39, v30, v24
	v_min_u32_e32 v40, v26, v23
	v_min_u32_e32 v41, v22, v18
	v_min_u32_e32 v42, v28, v34
	v_min_u32_e32 v14, v12, v9
	v_min_u32_e32 v8, v10, v3
	v_min_u32_e32 v13, v11, v5
	v_min_u32_e32 v6, v4, v2
	v_max3_u32 v23, v26, v23, v42
	v_max3_u32 v21, v21, v25, v14
	v_max3_u32 v8, v30, v24, v8
	v_max3_u32 v20, v20, v27, v13
	v_max3_u32 v6, v22, v18, v6
	v_max3_u32 v22, v31, v55, v49
	v_max3_u32 v24, v38, v47, v45
	v_max3_u32 v25, v36, v46, v48
	v_max3_u32 v27, v40, v28, v34
	v_max3_u32 v9, v35, v12, v9
	v_max3_u32 v3, v39, v10, v3
	v_max3_u32 v5, v37, v11, v5
	v_max3_u32 v2, v41, v4, v2
	v_min_u32_e32 v32, v19, v29
	v_min_u32_e32 v26, v33, v23
	v_min_u32_e32 v15, v21, v8
	v_min_u32_e32 v7, v20, v6
	v_min_u32_e32 v17, v22, v24
	v_min_u32_e32 v18, v25, v27
	v_min_u32_e32 v30, v9, v3
	v_min_u32_e32 v4, v5, v2
	v_min_u32_e32 v42, v32, v26
	v_min_u32_e32 v14, v15, v7
	v_min_u32_e32 v28, v17, v18
	v_min_u32_e32 v11, v30, v4
	v_min_u32_e32 v16, v42, v14
	v_min_u32_e32 v10, v28, v11
; __device__ __forceinline__ void merge_top16(uint32_t (&Lk)[16], const uint32_t (&K)[16]) {
; #pragma unroll
;   for (int i = 0; i < 16; ++i) Lk[i] = max(Lk[i], K[15 - i]);
; #pragma unroll
;   for (int dd = 8; dd >= 1; dd >>= 1)
; #pragma unroll
;     for (int i = 0; i < 16; ++i)
;       if ((i & dd) == 0) ce_desc(Lk[i], Lk[i + dd]);
; }
; __device__ void phase_q_route(KParams& p, int bid, int nb, char* smem) {
;     ...
; #pragma unroll
;       for (int i = 0; i < 8; ++i) {
;         const uint32_t t1 = (uint32_t)__shfl_xor((int)Lk[15 - i], 32), t2 = (uint32_t)__shfl_xor((int)Lk[i], 32);
;         Lk[i] = max(Lk[i], t1); Lk[15 - i] = max(Lk[15 - i], t2);
;       }
	v_max_u32_e32 v12, v42, v14
	v_max_u32_e32 v11, v28, v11
	v_min_u32_e32 v13, v16, v10
	v_max_u32_e32 v10, v16, v10
	v_min_u32_e32 v14, v12, v11
	v_max_u32_e32 v12, v12, v11
	v_max_u32_e32 v11, v32, v26
	v_max_u32_e32 v7, v15, v7
	v_max_u32_e32 v16, v17, v18
	v_max_u32_e32 v4, v30, v4
	v_min_u32_e32 v15, v11, v7
	v_min_u32_e32 v18, v16, v4
	v_max_u32_e32 v7, v11, v7
	v_max_u32_e32 v4, v16, v4
	v_min_u32_e32 v17, v15, v18
	v_max_u32_e32 v15, v15, v18
	v_min_u32_e32 v18, v7, v4
	v_max_u32_e32 v16, v7, v4
	v_max_u32_e32 v4, v19, v29
	v_max_u32_e32 v7, v33, v23
	v_max_u32_e32 v8, v21, v8
	v_max_u32_e32 v6, v20, v6
	v_max_u32_e32 v23, v22, v24
	v_max_u32_e32 v24, v25, v27
	v_max_u32_e32 v3, v9, v3
	v_max_u32_e32 v2, v5, v2
	v_min_u32_e32 v11, v4, v7
	v_min_u32_e32 v21, v8, v6
	v_min_u32_e32 v22, v23, v24
	v_min_u32_e32 v5, v3, v2
	v_min_u32_e32 v20, v11, v21
	v_min_u32_e32 v9, v22, v5
	v_min_u32_e32 v19, v20, v9
	v_max_u32_e32 v20, v20, v9
	v_max_u32_e32 v9, v11, v21
	v_max_u32_e32 v5, v22, v5
	v_min_u32_e32 v21, v9, v5
	v_max_u32_e32 v22, v9, v5
	v_max_u32_e32 v4, v4, v7
	v_max_u32_e32 v5, v8, v6
	v_max_u32_e32 v7, v23, v24
	v_max_u32_e32 v2, v3, v2
	v_min_u32_e32 v6, v4, v5
	v_min_u32_e32 v3, v7, v2
	v_min_u32_e32 v25, v6, v3
	v_max_u32_e32 v31, v6, v3
	ds_bpermute_b32 v24, v71, v13
	ds_bpermute_b32 v37, v71, v31
	ds_bpermute_b32 v38, v71, v12
	ds_bpermute_b32 v39, v71, v25
	ds_bpermute_b32 v40, v71, v17
	ds_bpermute_b32 v41, v71, v22
	v_max_u32_e32 v203, v206, v209
	v_min_u32_e32 v209, v206, v209
	v_max_u32_e32 v206, v66, v203
	v_min_u32_e32 v207, v66, v203
	v_min_u32_e32 v203, v199, v208
	v_min_u32_e32 v204, v205, v209
	v_max_u32_e32 v3, v4, v5
	v_max_u32_e32 v2, v7, v2
	v_max_u32_e32 v66, v200, v206
	v_max_u32_e32 v70, v202, v207
	v_min_u32_e32 v32, v3, v2
	v_max_u32_e32 v23, v3, v2
	v_max_u32_e32 v2, v203, v204
	ds_bpermute_b32 v33, v71, v23
	ds_bpermute_b32 v34, v71, v10
	ds_bpermute_b32 v35, v71, v32
	ds_bpermute_b32 v36, v71, v14
	ds_bpermute_b32 v42, v71, v15
	ds_bpermute_b32 v43, v71, v21
	ds_bpermute_b32 v44, v71, v18
	ds_bpermute_b32 v45, v71, v20
	ds_bpermute_b32 v46, v71, v16
	ds_bpermute_b32 v47, v71, v19
	s_waitcnt lgkmcnt(0)
	s_barrier
; __device__ void phase_q_route(KParams& p, int bid, int nb, char* smem) {
;     ...
; #pragma unroll
;       for (int i = 0; i < 8; ++i) {
;         const uint32_t t1 = (uint32_t)__shfl_xor((int)Lk[15 - i], 32), t2 = (uint32_t)__shfl_xor((int)Lk[i], 32);
;         Lk[i] = max(Lk[i], t1); Lk[15 - i] = max(Lk[15 - i], t2);
;       }
; #pragma unroll
;       for (int dd = 8; dd >= 1; dd >>= 1)
; #pragma unroll
;         for (int i = 0; i < 16; ++i)
;           if ((i & dd) == 0) { const uint32_t hi = max(Lk[i], Lk[i + dd]), lo = min(Lk[i], Lk[i + dd]); Lk[i] = hi; Lk[i + dd] = lo; }
; #pragma unroll
;       for (int r = 0; r < 16; ++r) { if (sd == 0) L1[r] = Lk[r]; else L2[r] = Lk[r]; }
;     }
;     __syncthreads();
;     uint32_t* ib = reinterpret_cast<uint32_t*>(smem) + w * 1088 + l31 * 34;
;     if (lh == 0) {
; #pragma unroll
;       for (int r = 0; r < 16; ++r) { ib[r] = L1[r] & 127u; ib[16 + r] = L2[r] & 127u; }
	s_and_saveexec_b64 s[48:49], s[8:9]
	s_xor_b64 s[48:49], exec, s[48:49]
	s_or_saveexec_b64 s[48:49], s[48:49]
	v_max_u32_e32 v13, v13, v33
	v_max_u32_e32 v32, v32, v34
	v_max_u32_e32 v10, v10, v35
	v_max_u32_e32 v31, v31, v36
	v_max_u32_e32 v14, v14, v37
	v_max_u32_e32 v25, v25, v38
	v_max_u32_e32 v12, v12, v39
	v_max_u32_e32 v22, v22, v40
	v_max_u32_e32 v17, v17, v41
	v_max_u32_e32 v21, v21, v42
	v_max_u32_e32 v15, v15, v43
	v_max_u32_e32 v20, v20, v44
	v_max_u32_e32 v18, v18, v45
	v_max_u32_e32 v19, v19, v46
	v_max_u32_e32 v16, v16, v47
	v_max_u32_e32 v23, v23, v24
	v_min_u32_e32 v3, v201, v198
	v_min_u32_e32 v4, v175, v197
	v_min_u32_e32 v5, v177, v194
	v_min_u32_e32 v6, v183, v192
	v_min_u32_e32 v7, v191, v185
	v_min_u32_e32 v8, v193, v176
	v_min_u32_e32 v9, v195, v73
	v_min_u32_e32 v11, v196, v72
	v_max_u32_e32 v24, v23, v16
	v_min_u32_e32 v16, v23, v16
	v_max_u32_e32 v23, v32, v18
	v_min_u32_e32 v18, v32, v18
	v_max_u32_e32 v32, v31, v15
	v_min_u32_e32 v15, v31, v15
	v_max_u32_e32 v31, v25, v17
	v_min_u32_e32 v17, v25, v17
	v_max_u32_e32 v25, v22, v12
	v_min_u32_e32 v12, v22, v12
	v_max_u32_e32 v22, v21, v14
	v_min_u32_e32 v14, v21, v14
	v_max_u32_e32 v21, v20, v10
	v_min_u32_e32 v10, v20, v10
	v_max_u32_e32 v20, v19, v13
	v_min_u32_e32 v13, v19, v13
	v_max_u32_e32 v26, v3, v7
	v_min_u32_e32 v3, v3, v7
	v_max_u32_e32 v7, v4, v8
	v_min_u32_e32 v4, v4, v8
	v_max_u32_e32 v8, v5, v9
	v_min_u32_e32 v5, v5, v9
	v_max_u32_e32 v9, v6, v11
	v_min_u32_e32 v6, v6, v11
	v_max_u32_e32 v19, v24, v25
	v_min_u32_e32 v24, v24, v25
	v_max_u32_e32 v25, v23, v22
	v_min_u32_e32 v22, v23, v22
	v_max_u32_e32 v23, v32, v21
	v_min_u32_e32 v21, v32, v21
	v_max_u32_e32 v32, v31, v20
	v_min_u32_e32 v20, v31, v20
	v_max_u32_e32 v31, v16, v12
	v_min_u32_e32 v12, v16, v12
	v_max_u32_e32 v16, v18, v14
	v_min_u32_e32 v14, v18, v14
	v_max_u32_e32 v18, v15, v10
	v_min_u32_e32 v10, v15, v10
	v_max_u32_e32 v15, v17, v13
	v_min_u32_e32 v13, v17, v13
	v_max_u32_e32 v11, v199, v208
	v_max_u32_e32 v27, v205, v209
	v_max_u32_e32 v28, v26, v8
	v_min_u32_e32 v26, v26, v8
	v_max_u32_e32 v29, v7, v9
	v_min_u32_e32 v48, v7, v9
	v_max_u32_e32 v49, v3, v5
	v_min_u32_e32 v50, v3, v5
	v_max_u32_e32 v3, v4, v6
	v_min_u32_e32 v4, v4, v6
	v_max_u32_e32 v17, v19, v23
	v_min_u32_e32 v19, v19, v23
	v_max_u32_e32 v23, v25, v32
	v_min_u32_e32 v25, v25, v32
	v_max_u32_e32 v32, v24, v21
	v_min_u32_e32 v21, v24, v21
	v_max_u32_e32 v24, v22, v20
	v_min_u32_e32 v33, v22, v20
	v_max_u32_e32 v34, v31, v18
	v_min_u32_e32 v31, v31, v18
	v_max_u32_e32 v35, v16, v15
	v_min_u32_e32 v15, v16, v15
	v_max_u32_e32 v16, v12, v10
	v_min_u32_e32 v36, v12, v10
	v_max_u32_e32 v42, v14, v13
	v_min_u32_e32 v14, v14, v13
	v_min_u32_e32 v6, v200, v206
	v_min_u32_e32 v9, v202, v207
	v_max_u32_e32 v8, v11, v27
	v_min_u32_e32 v7, v11, v27
	v_min_u32_e32 v5, v203, v204
	v_max_u32_e32 v30, v28, v29
	v_min_u32_e32 v29, v28, v29
	v_max_u32_e32 v28, v26, v48
	v_min_u32_e32 v27, v26, v48
	v_max_u32_e32 v26, v49, v3
	v_min_u32_e32 v11, v49, v3
	v_max_u32_e32 v3, v50, v4
	v_min_u32_e32 v4, v50, v4
	v_max_u32_e32 v18, v17, v23
	v_min_u32_e32 v23, v17, v23
	v_max_u32_e32 v12, v19, v25
	v_min_u32_e32 v10, v19, v25
	v_max_u32_e32 v20, v32, v24
	v_min_u32_e32 v13, v32, v24
	v_max_u32_e32 v22, v21, v33
	v_min_u32_e32 v24, v21, v33
	v_max_u32_e32 v41, v34, v35
	v_min_u32_e32 v40, v34, v35
	v_max_u32_e32 v39, v31, v15
	v_min_u32_e32 v38, v31, v15
	v_max_u32_e32 v37, v16, v42
	v_min_u32_e32 v21, v16, v42
	v_max_u32_e32 v25, v36, v14
	v_min_u32_e32 v19, v36, v14
	s_xor_b64 exec, exec, s[48:49]
	s_cbranch_execz .LBB0_1192
	v_and_b32_e32 v15, 0x7f, v6
	v_and_b32_e32 v14, 0x7f, v66
	v_and_b32_e32 v33, 0x7f, v9
	v_and_b32_e32 v32, 0x7f, v70
	v_and_b32_e32 v17, 0x7f, v23
	v_and_b32_e32 v16, 0x7f, v18
	v_and_b32_e32 v35, 0x7f, v10
	v_and_b32_e32 v34, 0x7f, v12
	ds_write2_b64 v78, v[14:15], v[32:33] offset1:1
	ds_write2_b64 v78, v[16:17], v[34:35] offset0:8 offset1:9
	v_and_b32_e32 v15, 0x7f, v7
	v_and_b32_e32 v14, 0x7f, v8
	v_and_b32_e32 v33, 0x7f, v5
	v_and_b32_e32 v32, 0x7f, v2
	v_and_b32_e32 v17, 0x7f, v13
	v_and_b32_e32 v16, 0x7f, v20
	v_and_b32_e32 v35, 0x7f, v24
	v_and_b32_e32 v34, 0x7f, v22
	ds_write2_b64 v78, v[14:15], v[32:33] offset0:2 offset1:3
	ds_write2_b64 v78, v[16:17], v[34:35] offset0:10 offset1:11
	v_and_b32_e32 v15, 0x7f, v29
	v_and_b32_e32 v14, 0x7f, v30
	v_and_b32_e32 v33, 0x7f, v27
	v_and_b32_e32 v32, 0x7f, v28
	v_and_b32_e32 v17, 0x7f, v40
	v_and_b32_e32 v16, 0x7f, v41
	v_and_b32_e32 v35, 0x7f, v38
	v_and_b32_e32 v34, 0x7f, v39
	ds_write2_b64 v78, v[14:15], v[32:33] offset0:4 offset1:5
	ds_write2_b64 v78, v[16:17], v[34:35] offset0:12 offset1:13
	v_and_b32_e32 v15, 0x7f, v11
	v_and_b32_e32 v14, 0x7f, v26
	v_and_b32_e32 v33, 0x7f, v4
	v_and_b32_e32 v32, 0x7f, v3
	v_and_b32_e32 v17, 0x7f, v21
	v_and_b32_e32 v16, 0x7f, v37
	v_and_b32_e32 v35, 0x7f, v19
	v_and_b32_e32 v34, 0x7f, v25
	ds_write2_b64 v78, v[14:15], v[32:33] offset0:6 offset1:7
	ds_write2_b64 v78, v[16:17], v[34:35] offset0:14 offset1:15
